# baseline (speedup 1.0000x reference)
.Lou_loop:
	s_waitcnt lgkmcnt(0)
	v_mfma_f32_16x16x32_bf16 v[64:67], v[176:179], v[160:163], v[64:67]
	ds_read_b128 v[200:203], v11 offset:0
	v_mfma_f32_16x16x32_bf16 v[68:71], v[176:179], v[164:167], v[68:71]
	ds_read_b128 v[204:207], v11 offset:2048
	v_mfma_f32_16x16x32_bf16 v[72:75], v[176:179], v[168:171], v[72:75]
	ds_read_b128 v[208:211], v11 offset:4096
	v_mfma_f32_16x16x32_bf16 v[76:79], v[176:179], v[172:175], v[76:79]
	ds_read_b128 v[212:215], v11 offset:6144
	v_mfma_f32_16x16x32_bf16 v[80:83], v[180:183], v[160:163], v[80:83]
	ds_read_b128 v[216:219], v13 offset:0
	v_mfma_f32_16x16x32_bf16 v[84:87], v[180:183], v[164:167], v[84:87]
	ds_read_b128 v[220:223], v13 offset:2048
	v_mfma_f32_16x16x32_bf16 v[88:91], v[180:183], v[168:171], v[88:91]
	ds_read_b128 v[224:227], v13 offset:4096
	v_mfma_f32_16x16x32_bf16 v[92:95], v[180:183], v[172:175], v[92:95]
	ds_read_b128 v[228:231], v13 offset:6144
	v_mfma_f32_16x16x32_bf16 v[96:99], v[184:187], v[160:163], v[96:99]
	ds_read_b128 v[232:235], v13 offset:8192
	v_mfma_f32_16x16x32_bf16 v[100:103], v[184:187], v[164:167], v[100:103]
	ds_read_b128 v[236:239], v13 offset:10240
	v_mfma_f32_16x16x32_bf16 v[104:107], v[184:187], v[168:171], v[104:107]
	s_add_u32 m0, s20, 0x5000
	v_mfma_f32_16x16x32_bf16 v[108:111], v[184:187], v[172:175], v[108:111]
	global_load_lds_dwordx4 v3, s[18:19]
	v_mfma_f32_16x16x32_bf16 v[112:115], v[188:191], v[160:163], v[112:115]
	s_add_u32 m0, s20, 0x6000
	v_mfma_f32_16x16x32_bf16 v[116:119], v[188:191], v[164:167], v[116:119]
	global_load_lds_dwordx4 v4, s[18:19]
	v_mfma_f32_16x16x32_bf16 v[120:123], v[188:191], v[168:171], v[120:123]
	s_add_u32 m0, s20, 0x7000
	v_mfma_f32_16x16x32_bf16 v[124:127], v[188:191], v[172:175], v[124:127]
	global_load_lds_dwordx4 v5, s[18:19]
	v_mfma_f32_16x16x32_bf16 v[128:131], v[192:195], v[160:163], v[128:131]
	s_add_u32 m0, s20, 0x8000
	v_mfma_f32_16x16x32_bf16 v[132:135], v[192:195], v[164:167], v[132:135]
	global_load_lds_dwordx4 v6, s[18:19]
	v_mfma_f32_16x16x32_bf16 v[136:139], v[192:195], v[168:171], v[136:139]
	s_add_u32 m0, s20, 0x9000
	v_mfma_f32_16x16x32_bf16 v[140:143], v[192:195], v[172:175], v[140:143]
	global_load_lds_dwordx4 v7, s[18:19]
	v_mfma_f32_16x16x32_bf16 v[144:147], v[196:199], v[160:163], v[144:147]
	s_add_u32 s16, s16, 0x80
	s_addc_u32 s17, s17, 0
	s_add_u32 s18, s18, 0x80
	s_addc_u32 s19, s19, 0
	v_mfma_f32_16x16x32_bf16 v[148:151], v[196:199], v[164:167], v[148:151]
	s_add_u32 s20, s20, 0xa000
	s_sub_u32 s22, s20, 0x28000
	s_cmp_ge_u32 s20, 0x28000
	s_cselect_b32 s20, s22, s20
	v_mfma_f32_16x16x32_bf16 v[152:155], v[196:199], v[168:171], v[152:155]
	v_add_u32_e32 v10, s21, v8
	v_add_u32_e32 v12, s21, v9
	v_xor_b32_e32 v11, 64, v10
	v_xor_b32_e32 v13, 64, v12
	v_mfma_f32_16x16x32_bf16 v[156:159], v[196:199], v[172:175], v[156:159]
	s_add_u32 s21, s21, 0xa000
	s_sub_u32 s23, s21, 0x28000
	s_cmp_ge_u32 s21, 0x28000
	s_cselect_b32 s21, s23, s21
	s_waitcnt lgkmcnt(0)
	v_mfma_f32_16x16x32_bf16 v[64:67], v[216:219], v[200:203], v[64:67]
	v_mfma_f32_16x16x32_bf16 v[68:71], v[216:219], v[204:207], v[68:71]
	v_mfma_f32_16x16x32_bf16 v[72:75], v[216:219], v[208:211], v[72:75]
	v_mfma_f32_16x16x32_bf16 v[76:79], v[216:219], v[212:215], v[76:79]
	s_waitcnt vmcnt(20)
	s_barrier
	v_mfma_f32_16x16x32_bf16 v[80:83], v[220:223], v[200:203], v[80:83]
	ds_read_b128 v[160:163], v10 offset:0
	v_mfma_f32_16x16x32_bf16 v[84:87], v[220:223], v[204:207], v[84:87]
	ds_read_b128 v[164:167], v10 offset:2048
	v_mfma_f32_16x16x32_bf16 v[88:91], v[220:223], v[208:211], v[88:91]
	ds_read_b128 v[168:171], v10 offset:4096
	v_mfma_f32_16x16x32_bf16 v[92:95], v[220:223], v[212:215], v[92:95]
	ds_read_b128 v[172:175], v10 offset:6144
	v_mfma_f32_16x16x32_bf16 v[96:99], v[224:227], v[200:203], v[96:99]
	ds_read_b128 v[176:179], v12 offset:0
	v_mfma_f32_16x16x32_bf16 v[100:103], v[224:227], v[204:207], v[100:103]
	ds_read_b128 v[180:183], v12 offset:2048
	v_mfma_f32_16x16x32_bf16 v[104:107], v[224:227], v[208:211], v[104:107]
	ds_read_b128 v[184:187], v12 offset:4096
	v_mfma_f32_16x16x32_bf16 v[108:111], v[224:227], v[212:215], v[108:111]
	ds_read_b128 v[188:191], v12 offset:6144
	v_mfma_f32_16x16x32_bf16 v[112:115], v[228:231], v[200:203], v[112:115]
	ds_read_b128 v[192:195], v12 offset:8192
	v_mfma_f32_16x16x32_bf16 v[116:119], v[228:231], v[204:207], v[116:119]
	ds_read_b128 v[196:199], v12 offset:10240
	v_mfma_f32_16x16x32_bf16 v[120:123], v[228:231], v[208:211], v[120:123]
	s_add_u32 m0, s20, 0x0
	v_mfma_f32_16x16x32_bf16 v[124:127], v[228:231], v[212:215], v[124:127]
	global_load_lds_dwordx4 v2, s[16:17]
	v_mfma_f32_16x16x32_bf16 v[128:131], v[232:235], v[200:203], v[128:131]
	s_add_u32 m0, s20, 0x1000
	v_mfma_f32_16x16x32_bf16 v[132:135], v[232:235], v[204:207], v[132:135]
	global_load_lds_dwordx4 v3, s[16:17]
	v_mfma_f32_16x16x32_bf16 v[136:139], v[232:235], v[208:211], v[136:139]
	s_add_u32 m0, s20, 0x2000
	v_mfma_f32_16x16x32_bf16 v[140:143], v[232:235], v[212:215], v[140:143]
	global_load_lds_dwordx4 v4, s[16:17]
	v_mfma_f32_16x16x32_bf16 v[144:147], v[236:239], v[200:203], v[144:147]
	s_add_u32 m0, s20, 0x3000
	v_mfma_f32_16x16x32_bf16 v[148:151], v[236:239], v[204:207], v[148:151]
	global_load_lds_dwordx4 v5, s[16:17]
	v_mfma_f32_16x16x32_bf16 v[152:155], v[236:239], v[208:211], v[152:155]
	s_add_u32 m0, s20, 0x4000
	v_mfma_f32_16x16x32_bf16 v[156:159], v[236:239], v[212:215], v[156:159]
	global_load_lds_dwordx4 v2, s[18:19]
	s_add_u32 s15, s15, 1
	s_cmp_lt_u32 s15, 8
	s_cbranch_scc1 .Lou_loop
	s_waitcnt lgkmcnt(0)
	v_mfma_f32_16x16x32_bf16 v[64:67], v[176:179], v[160:163], v[64:67]
	ds_read_b128 v[200:203], v11 offset:0
	v_mfma_f32_16x16x32_bf16 v[68:71], v[176:179], v[164:167], v[68:71]
	ds_read_b128 v[204:207], v11 offset:2048
	v_mfma_f32_16x16x32_bf16 v[72:75], v[176:179], v[168:171], v[72:75]
	ds_read_b128 v[208:211], v11 offset:4096
	v_mfma_f32_16x16x32_bf16 v[76:79], v[176:179], v[172:175], v[76:79]
	ds_read_b128 v[212:215], v11 offset:6144
	v_mfma_f32_16x16x32_bf16 v[80:83], v[180:183], v[160:163], v[80:83]
	ds_read_b128 v[216:219], v13 offset:0
	v_mfma_f32_16x16x32_bf16 v[84:87], v[180:183], v[164:167], v[84:87]
	ds_read_b128 v[220:223], v13 offset:2048
	v_mfma_f32_16x16x32_bf16 v[88:91], v[180:183], v[168:171], v[88:91]
	ds_read_b128 v[224:227], v13 offset:4096
	v_mfma_f32_16x16x32_bf16 v[92:95], v[180:183], v[172:175], v[92:95]
	ds_read_b128 v[228:231], v13 offset:6144
	v_mfma_f32_16x16x32_bf16 v[96:99], v[184:187], v[160:163], v[96:99]
	ds_read_b128 v[232:235], v13 offset:8192
	v_mfma_f32_16x16x32_bf16 v[100:103], v[184:187], v[164:167], v[100:103]
	ds_read_b128 v[236:239], v13 offset:10240
	v_mfma_f32_16x16x32_bf16 v[104:107], v[184:187], v[168:171], v[104:107]
	s_add_u32 m0, s20, 0x5000
	v_mfma_f32_16x16x32_bf16 v[108:111], v[184:187], v[172:175], v[108:111]
	global_load_lds_dwordx4 v3, s[18:19]
	v_mfma_f32_16x16x32_bf16 v[112:115], v[188:191], v[160:163], v[112:115]
	s_add_u32 m0, s20, 0x6000
	v_mfma_f32_16x16x32_bf16 v[116:119], v[188:191], v[164:167], v[116:119]
	global_load_lds_dwordx4 v4, s[18:19]
	v_mfma_f32_16x16x32_bf16 v[120:123], v[188:191], v[168:171], v[120:123]
	s_add_u32 m0, s20, 0x7000
	v_mfma_f32_16x16x32_bf16 v[124:127], v[188:191], v[172:175], v[124:127]
	global_load_lds_dwordx4 v5, s[18:19]
	v_mfma_f32_16x16x32_bf16 v[128:131], v[192:195], v[160:163], v[128:131]
	s_add_u32 m0, s20, 0x8000
	v_mfma_f32_16x16x32_bf16 v[132:135], v[192:195], v[164:167], v[132:135]
	global_load_lds_dwordx4 v6, s[18:19]
	v_mfma_f32_16x16x32_bf16 v[136:139], v[192:195], v[168:171], v[136:139]
	s_add_u32 m0, s20, 0x9000
	v_mfma_f32_16x16x32_bf16 v[140:143], v[192:195], v[172:175], v[140:143]
	global_load_lds_dwordx4 v7, s[18:19]
	v_mfma_f32_16x16x32_bf16 v[144:147], v[196:199], v[160:163], v[144:147]
	s_add_u32 s16, s16, 0x80
	s_addc_u32 s17, s17, 0
	s_add_u32 s18, s18, 0x80
	s_addc_u32 s19, s19, 0
	v_mfma_f32_16x16x32_bf16 v[148:151], v[196:199], v[164:167], v[148:151]
	s_add_u32 s20, s20, 0xa000
	s_sub_u32 s22, s20, 0x28000
	s_cmp_ge_u32 s20, 0x28000
	s_cselect_b32 s20, s22, s20
	v_mfma_f32_16x16x32_bf16 v[152:155], v[196:199], v[168:171], v[152:155]
	v_add_u32_e32 v10, s21, v8
	v_add_u32_e32 v12, s21, v9
	v_xor_b32_e32 v11, 64, v10
	v_xor_b32_e32 v13, 64, v12
	v_mfma_f32_16x16x32_bf16 v[156:159], v[196:199], v[172:175], v[156:159]
	s_add_u32 s21, s21, 0xa000
	s_sub_u32 s23, s21, 0x28000
	s_cmp_ge_u32 s21, 0x28000
	s_cselect_b32 s21, s23, s21
	s_waitcnt lgkmcnt(0)
	v_mfma_f32_16x16x32_bf16 v[64:67], v[216:219], v[200:203], v[64:67]
	v_mfma_f32_16x16x32_bf16 v[68:71], v[216:219], v[204:207], v[68:71]
	v_mfma_f32_16x16x32_bf16 v[72:75], v[216:219], v[208:211], v[72:75]
	v_mfma_f32_16x16x32_bf16 v[76:79], v[216:219], v[212:215], v[76:79]
	s_waitcnt vmcnt(20)
	s_barrier
	v_mfma_f32_16x16x32_bf16 v[80:83], v[220:223], v[200:203], v[80:83]
	ds_read_b128 v[160:163], v10 offset:0
	v_mfma_f32_16x16x32_bf16 v[84:87], v[220:223], v[204:207], v[84:87]
	ds_read_b128 v[164:167], v10 offset:2048
	v_mfma_f32_16x16x32_bf16 v[88:91], v[220:223], v[208:211], v[88:91]
	ds_read_b128 v[168:171], v10 offset:4096
	v_mfma_f32_16x16x32_bf16 v[92:95], v[220:223], v[212:215], v[92:95]
	ds_read_b128 v[172:175], v10 offset:6144
	v_mfma_f32_16x16x32_bf16 v[96:99], v[224:227], v[200:203], v[96:99]
	ds_read_b128 v[176:179], v12 offset:0
	v_mfma_f32_16x16x32_bf16 v[100:103], v[224:227], v[204:207], v[100:103]
	ds_read_b128 v[180:183], v12 offset:2048
	v_mfma_f32_16x16x32_bf16 v[104:107], v[224:227], v[208:211], v[104:107]
	ds_read_b128 v[184:187], v12 offset:4096
	v_mfma_f32_16x16x32_bf16 v[108:111], v[224:227], v[212:215], v[108:111]
	ds_read_b128 v[188:191], v12 offset:6144
	v_mfma_f32_16x16x32_bf16 v[112:115], v[228:231], v[200:203], v[112:115]
	ds_read_b128 v[192:195], v12 offset:8192
	v_mfma_f32_16x16x32_bf16 v[116:119], v[228:231], v[204:207], v[116:119]
	ds_read_b128 v[196:199], v12 offset:10240
	v_mfma_f32_16x16x32_bf16 v[120:123], v[228:231], v[208:211], v[120:123]
	global_load_dwordx4 v[240:243], v60, s[24:25]
	v_mfma_f32_16x16x32_bf16 v[124:127], v[228:231], v[212:215], v[124:127]
	global_load_dwordx4 v[244:247], v60, s[24:25] offset:64
	v_mfma_f32_16x16x32_bf16 v[128:131], v[232:235], v[200:203], v[128:131]
	global_load_dwordx4 v[248:251], v60, s[24:25] offset:128
	v_mfma_f32_16x16x32_bf16 v[132:135], v[232:235], v[204:207], v[132:135]
	global_load_dwordx4 v[252:255], v60, s[24:25] offset:192
	v_mfma_f32_16x16x32_bf16 v[136:139], v[232:235], v[208:211], v[136:139]
	global_load_dwordx4 v[48:51], v60, s[24:25] offset:256
	v_mfma_f32_16x16x32_bf16 v[140:143], v[232:235], v[212:215], v[140:143]
	global_load_dwordx4 v[52:55], v60, s[24:25] offset:320
	v_mfma_f32_16x16x32_bf16 v[144:147], v[236:239], v[200:203], v[144:147]
	global_load_dwordx4 v[16:19], v56, s[8:9] offset:0
	v_mfma_f32_16x16x32_bf16 v[148:151], v[236:239], v[204:207], v[148:151]
	global_load_dwordx4 v[20:23], v56, s[8:9] offset:64
	v_mfma_f32_16x16x32_bf16 v[152:155], v[236:239], v[208:211], v[152:155]
	global_load_dwordx4 v[24:27], v56, s[8:9] offset:128
	v_mfma_f32_16x16x32_bf16 v[156:159], v[236:239], v[212:215], v[156:159]
	global_load_dwordx4 v[28:31], v56, s[8:9] offset:192
	global_load_dwordx4 v[32:35], v56, s[8:9] offset:256
	global_load_dwordx4 v[36:39], v56, s[8:9] offset:320
	global_load_dwordx4 v[40:43], v57, s[8:9] offset:0
	global_load_dwordx4 v[44:47], v57, s[8:9] offset:64
	s_waitcnt lgkmcnt(0)
	v_mfma_f32_16x16x32_bf16 v[64:67], v[176:179], v[160:163], v[64:67]
	ds_read_b128 v[200:203], v11 offset:0
	v_mfma_f32_16x16x32_bf16 v[68:71], v[176:179], v[164:167], v[68:71]
	ds_read_b128 v[204:207], v11 offset:2048
	v_mfma_f32_16x16x32_bf16 v[72:75], v[176:179], v[168:171], v[72:75]
	ds_read_b128 v[208:211], v11 offset:4096
	v_mfma_f32_16x16x32_bf16 v[76:79], v[176:179], v[172:175], v[76:79]
	ds_read_b128 v[212:215], v11 offset:6144
	v_mfma_f32_16x16x32_bf16 v[80:83], v[180:183], v[160:163], v[80:83]
	ds_read_b128 v[216:219], v13 offset:0
	v_mfma_f32_16x16x32_bf16 v[84:87], v[180:183], v[164:167], v[84:87]
	ds_read_b128 v[220:223], v13 offset:2048
	v_mfma_f32_16x16x32_bf16 v[88:91], v[180:183], v[168:171], v[88:91]
	ds_read_b128 v[224:227], v13 offset:4096
	v_mfma_f32_16x16x32_bf16 v[92:95], v[180:183], v[172:175], v[92:95]
	ds_read_b128 v[228:231], v13 offset:6144
	v_mfma_f32_16x16x32_bf16 v[96:99], v[184:187], v[160:163], v[96:99]
	ds_read_b128 v[232:235], v13 offset:8192
	v_mfma_f32_16x16x32_bf16 v[100:103], v[184:187], v[164:167], v[100:103]
	ds_read_b128 v[236:239], v13 offset:10240
	v_mfma_f32_16x16x32_bf16 v[104:107], v[184:187], v[168:171], v[104:107]
	v_mfma_f32_16x16x32_bf16 v[108:111], v[184:187], v[172:175], v[108:111]
	v_mfma_f32_16x16x32_bf16 v[112:115], v[188:191], v[160:163], v[112:115]
	v_mfma_f32_16x16x32_bf16 v[116:119], v[188:191], v[164:167], v[116:119]
	v_mfma_f32_16x16x32_bf16 v[120:123], v[188:191], v[168:171], v[120:123]
	v_mfma_f32_16x16x32_bf16 v[124:127], v[188:191], v[172:175], v[124:127]
	v_mfma_f32_16x16x32_bf16 v[128:131], v[192:195], v[160:163], v[128:131]
	v_mfma_f32_16x16x32_bf16 v[132:135], v[192:195], v[164:167], v[132:135]
	v_mfma_f32_16x16x32_bf16 v[136:139], v[192:195], v[168:171], v[136:139]
	v_mfma_f32_16x16x32_bf16 v[140:143], v[192:195], v[172:175], v[140:143]
	v_mfma_f32_16x16x32_bf16 v[144:147], v[196:199], v[160:163], v[144:147]
	v_add_u32_e32 v10, s21, v8
	v_add_u32_e32 v12, s21, v9
	v_xor_b32_e32 v11, 64, v10
	v_xor_b32_e32 v13, 64, v12
	v_mfma_f32_16x16x32_bf16 v[148:151], v[196:199], v[164:167], v[148:151]
	s_add_u32 s21, s21, 0xa000
	s_sub_u32 s23, s21, 0x28000
	s_cmp_ge_u32 s21, 0x28000
	s_cselect_b32 s21, s23, s21
	v_mfma_f32_16x16x32_bf16 v[152:155], v[196:199], v[168:171], v[152:155]
	v_mfma_f32_16x16x32_bf16 v[156:159], v[196:199], v[172:175], v[156:159]
	s_waitcnt lgkmcnt(0)
	v_mfma_f32_16x16x32_bf16 v[64:67], v[216:219], v[200:203], v[64:67]
	v_mfma_f32_16x16x32_bf16 v[68:71], v[216:219], v[204:207], v[68:71]
	v_mfma_f32_16x16x32_bf16 v[72:75], v[216:219], v[208:211], v[72:75]
	v_mfma_f32_16x16x32_bf16 v[76:79], v[216:219], v[212:215], v[76:79]
	s_waitcnt vmcnt(24)
	s_barrier
	v_mfma_f32_16x16x32_bf16 v[80:83], v[220:223], v[200:203], v[80:83]
	ds_read_b128 v[160:163], v10 offset:0
	v_mfma_f32_16x16x32_bf16 v[84:87], v[220:223], v[204:207], v[84:87]
	ds_read_b128 v[164:167], v10 offset:2048
	v_mfma_f32_16x16x32_bf16 v[88:91], v[220:223], v[208:211], v[88:91]
	ds_read_b128 v[168:171], v10 offset:4096
	v_mfma_f32_16x16x32_bf16 v[92:95], v[220:223], v[212:215], v[92:95]
	ds_read_b128 v[172:175], v10 offset:6144
	v_mfma_f32_16x16x32_bf16 v[96:99], v[224:227], v[200:203], v[96:99]
	ds_read_b128 v[176:179], v12 offset:0
	v_mfma_f32_16x16x32_bf16 v[100:103], v[224:227], v[204:207], v[100:103]
	ds_read_b128 v[180:183], v12 offset:2048
	v_mfma_f32_16x16x32_bf16 v[104:107], v[224:227], v[208:211], v[104:107]
	ds_read_b128 v[184:187], v12 offset:4096
	v_mfma_f32_16x16x32_bf16 v[108:111], v[224:227], v[212:215], v[108:111]
	ds_read_b128 v[188:191], v12 offset:6144
	v_mfma_f32_16x16x32_bf16 v[112:115], v[228:231], v[200:203], v[112:115]
	ds_read_b128 v[192:195], v12 offset:8192
	v_mfma_f32_16x16x32_bf16 v[116:119], v[228:231], v[204:207], v[116:119]
	ds_read_b128 v[196:199], v12 offset:10240
	v_mfma_f32_16x16x32_bf16 v[120:123], v[228:231], v[208:211], v[120:123]
	v_mfma_f32_16x16x32_bf16 v[124:127], v[228:231], v[212:215], v[124:127]
	v_mfma_f32_16x16x32_bf16 v[128:131], v[232:235], v[200:203], v[128:131]
	v_mfma_f32_16x16x32_bf16 v[132:135], v[232:235], v[204:207], v[132:135]
	v_mfma_f32_16x16x32_bf16 v[136:139], v[232:235], v[208:211], v[136:139]
	v_mfma_f32_16x16x32_bf16 v[140:143], v[232:235], v[212:215], v[140:143]
	v_mfma_f32_16x16x32_bf16 v[144:147], v[236:239], v[200:203], v[144:147]
	v_mfma_f32_16x16x32_bf16 v[148:151], v[236:239], v[204:207], v[148:151]
	v_mfma_f32_16x16x32_bf16 v[152:155], v[236:239], v[208:211], v[152:155]
	v_mfma_f32_16x16x32_bf16 v[156:159], v[236:239], v[212:215], v[156:159]
	s_waitcnt lgkmcnt(0)
	v_mfma_f32_16x16x32_bf16 v[64:67], v[176:179], v[160:163], v[64:67]
	ds_read_b128 v[200:203], v11 offset:0
	v_mfma_f32_16x16x32_bf16 v[68:71], v[176:179], v[164:167], v[68:71]
	ds_read_b128 v[204:207], v11 offset:2048
	v_mfma_f32_16x16x32_bf16 v[72:75], v[176:179], v[168:171], v[72:75]
	ds_read_b128 v[208:211], v11 offset:4096
	v_mfma_f32_16x16x32_bf16 v[76:79], v[176:179], v[172:175], v[76:79]
	ds_read_b128 v[212:215], v11 offset:6144
	v_mfma_f32_16x16x32_bf16 v[80:83], v[180:183], v[160:163], v[80:83]
	ds_read_b128 v[216:219], v13 offset:0
	v_mfma_f32_16x16x32_bf16 v[84:87], v[180:183], v[164:167], v[84:87]
	ds_read_b128 v[220:223], v13 offset:2048
	v_mfma_f32_16x16x32_bf16 v[88:91], v[180:183], v[168:171], v[88:91]
	ds_read_b128 v[224:227], v13 offset:4096
	v_mfma_f32_16x16x32_bf16 v[92:95], v[180:183], v[172:175], v[92:95]
	ds_read_b128 v[228:231], v13 offset:6144
	v_mfma_f32_16x16x32_bf16 v[96:99], v[184:187], v[160:163], v[96:99]
	ds_read_b128 v[232:235], v13 offset:8192
	v_mfma_f32_16x16x32_bf16 v[100:103], v[184:187], v[164:167], v[100:103]
	ds_read_b128 v[236:239], v13 offset:10240
	v_mfma_f32_16x16x32_bf16 v[104:107], v[184:187], v[168:171], v[104:107]
	v_mfma_f32_16x16x32_bf16 v[108:111], v[184:187], v[172:175], v[108:111]
	v_mfma_f32_16x16x32_bf16 v[112:115], v[188:191], v[160:163], v[112:115]
	v_mfma_f32_16x16x32_bf16 v[116:119], v[188:191], v[164:167], v[116:119]
	v_mfma_f32_16x16x32_bf16 v[120:123], v[188:191], v[168:171], v[120:123]
	v_mfma_f32_16x16x32_bf16 v[124:127], v[188:191], v[172:175], v[124:127]
	v_mfma_f32_16x16x32_bf16 v[128:131], v[192:195], v[160:163], v[128:131]
	v_mfma_f32_16x16x32_bf16 v[132:135], v[192:195], v[164:167], v[132:135]
	v_mfma_f32_16x16x32_bf16 v[136:139], v[192:195], v[168:171], v[136:139]
	v_mfma_f32_16x16x32_bf16 v[140:143], v[192:195], v[172:175], v[140:143]
	v_mfma_f32_16x16x32_bf16 v[144:147], v[196:199], v[160:163], v[144:147]
	v_add_u32_e32 v10, s21, v8
	v_add_u32_e32 v12, s21, v9
	v_xor_b32_e32 v11, 64, v10
	v_xor_b32_e32 v13, 64, v12
	v_mfma_f32_16x16x32_bf16 v[148:151], v[196:199], v[164:167], v[148:151]
	s_add_u32 s21, s21, 0xa000
	s_sub_u32 s23, s21, 0x28000
	s_cmp_ge_u32 s21, 0x28000
	s_cselect_b32 s21, s23, s21
	v_mfma_f32_16x16x32_bf16 v[152:155], v[196:199], v[168:171], v[152:155]
	v_mfma_f32_16x16x32_bf16 v[156:159], v[196:199], v[172:175], v[156:159]
	s_waitcnt lgkmcnt(0)
	v_mfma_f32_16x16x32_bf16 v[64:67], v[216:219], v[200:203], v[64:67]
	v_mfma_f32_16x16x32_bf16 v[68:71], v[216:219], v[204:207], v[68:71]
	v_mfma_f32_16x16x32_bf16 v[72:75], v[216:219], v[208:211], v[72:75]
	v_mfma_f32_16x16x32_bf16 v[76:79], v[216:219], v[212:215], v[76:79]
	s_waitcnt vmcnt(14)
	s_barrier
	v_mfma_f32_16x16x32_bf16 v[80:83], v[220:223], v[200:203], v[80:83]
	ds_read_b128 v[160:163], v10 offset:0
	v_mfma_f32_16x16x32_bf16 v[84:87], v[220:223], v[204:207], v[84:87]
	ds_read_b128 v[164:167], v10 offset:2048
	v_mfma_f32_16x16x32_bf16 v[88:91], v[220:223], v[208:211], v[88:91]
	ds_read_b128 v[168:171], v10 offset:4096
	v_mfma_f32_16x16x32_bf16 v[92:95], v[220:223], v[212:215], v[92:95]
	ds_read_b128 v[172:175], v10 offset:6144
	v_mfma_f32_16x16x32_bf16 v[96:99], v[224:227], v[200:203], v[96:99]
	ds_read_b128 v[176:179], v12 offset:0
	v_mfma_f32_16x16x32_bf16 v[100:103], v[224:227], v[204:207], v[100:103]
	ds_read_b128 v[180:183], v12 offset:2048
	v_mfma_f32_16x16x32_bf16 v[104:107], v[224:227], v[208:211], v[104:107]
	ds_read_b128 v[184:187], v12 offset:4096
	v_mfma_f32_16x16x32_bf16 v[108:111], v[224:227], v[212:215], v[108:111]
	ds_read_b128 v[188:191], v12 offset:6144
	v_mfma_f32_16x16x32_bf16 v[112:115], v[228:231], v[200:203], v[112:115]
	ds_read_b128 v[192:195], v12 offset:8192
	v_mfma_f32_16x16x32_bf16 v[116:119], v[228:231], v[204:207], v[116:119]
	ds_read_b128 v[196:199], v12 offset:10240
	v_mfma_f32_16x16x32_bf16 v[120:123], v[228:231], v[208:211], v[120:123]
	v_mfma_f32_16x16x32_bf16 v[124:127], v[228:231], v[212:215], v[124:127]
	v_mfma_f32_16x16x32_bf16 v[128:131], v[232:235], v[200:203], v[128:131]
	v_mfma_f32_16x16x32_bf16 v[132:135], v[232:235], v[204:207], v[132:135]
	v_mfma_f32_16x16x32_bf16 v[136:139], v[232:235], v[208:211], v[136:139]
	v_mfma_f32_16x16x32_bf16 v[140:143], v[232:235], v[212:215], v[140:143]
	v_mfma_f32_16x16x32_bf16 v[144:147], v[236:239], v[200:203], v[144:147]
	v_mfma_f32_16x16x32_bf16 v[148:151], v[236:239], v[204:207], v[148:151]
	v_mfma_f32_16x16x32_bf16 v[152:155], v[236:239], v[208:211], v[152:155]
	v_mfma_f32_16x16x32_bf16 v[156:159], v[236:239], v[212:215], v[156:159]
	s_waitcnt lgkmcnt(0)
	v_mfma_f32_16x16x32_bf16 v[64:67], v[176:179], v[160:163], v[64:67]
	ds_read_b128 v[200:203], v11 offset:0
	v_mfma_f32_16x16x32_bf16 v[68:71], v[176:179], v[164:167], v[68:71]
	ds_read_b128 v[204:207], v11 offset:2048
	v_mfma_f32_16x16x32_bf16 v[72:75], v[176:179], v[168:171], v[72:75]
	ds_read_b128 v[208:211], v11 offset:4096
	v_mfma_f32_16x16x32_bf16 v[76:79], v[176:179], v[172:175], v[76:79]
	ds_read_b128 v[212:215], v11 offset:6144
	v_mfma_f32_16x16x32_bf16 v[80:83], v[180:183], v[160:163], v[80:83]
	ds_read_b128 v[216:219], v13 offset:0
	v_mfma_f32_16x16x32_bf16 v[84:87], v[180:183], v[164:167], v[84:87]
	ds_read_b128 v[220:223], v13 offset:2048
	v_mfma_f32_16x16x32_bf16 v[88:91], v[180:183], v[168:171], v[88:91]
	ds_read_b128 v[224:227], v13 offset:4096
	v_mfma_f32_16x16x32_bf16 v[92:95], v[180:183], v[172:175], v[92:95]
	ds_read_b128 v[228:231], v13 offset:6144
	v_mfma_f32_16x16x32_bf16 v[96:99], v[184:187], v[160:163], v[96:99]
	ds_read_b128 v[232:235], v13 offset:8192
	v_mfma_f32_16x16x32_bf16 v[100:103], v[184:187], v[164:167], v[100:103]
	ds_read_b128 v[236:239], v13 offset:10240
	v_mfma_f32_16x16x32_bf16 v[104:107], v[184:187], v[168:171], v[104:107]
	v_mfma_f32_16x16x32_bf16 v[108:111], v[184:187], v[172:175], v[108:111]
	v_mfma_f32_16x16x32_bf16 v[112:115], v[188:191], v[160:163], v[112:115]
	v_mfma_f32_16x16x32_bf16 v[116:119], v[188:191], v[164:167], v[116:119]
	v_mfma_f32_16x16x32_bf16 v[120:123], v[188:191], v[168:171], v[120:123]
	v_mfma_f32_16x16x32_bf16 v[124:127], v[188:191], v[172:175], v[124:127]
	v_mfma_f32_16x16x32_bf16 v[128:131], v[192:195], v[160:163], v[128:131]
	v_mfma_f32_16x16x32_bf16 v[132:135], v[192:195], v[164:167], v[132:135]
	v_mfma_f32_16x16x32_bf16 v[136:139], v[192:195], v[168:171], v[136:139]
	v_mfma_f32_16x16x32_bf16 v[140:143], v[192:195], v[172:175], v[140:143]
	v_mfma_f32_16x16x32_bf16 v[144:147], v[196:199], v[160:163], v[144:147]
	v_mfma_f32_16x16x32_bf16 v[148:151], v[196:199], v[164:167], v[148:151]
	v_mfma_f32_16x16x32_bf16 v[152:155], v[196:199], v[168:171], v[152:155]
	v_mfma_f32_16x16x32_bf16 v[156:159], v[196:199], v[172:175], v[156:159]
	s_waitcnt lgkmcnt(0)
	v_mfma_f32_16x16x32_bf16 v[64:67], v[216:219], v[200:203], v[64:67]
	v_mfma_f32_16x16x32_bf16 v[68:71], v[216:219], v[204:207], v[68:71]
	global_load_dwordx4 v[160:163], v57, s[8:9] offset:128
	v_mfma_f32_16x16x32_bf16 v[72:75], v[216:219], v[208:211], v[72:75]
	v_mfma_f32_16x16x32_bf16 v[76:79], v[216:219], v[212:215], v[76:79]
	global_load_dwordx4 v[164:167], v57, s[8:9] offset:192
	v_mfma_f32_16x16x32_bf16 v[80:83], v[220:223], v[200:203], v[80:83]
	v_mfma_f32_16x16x32_bf16 v[84:87], v[220:223], v[204:207], v[84:87]
	global_load_dwordx4 v[168:171], v57, s[8:9] offset:256
	v_mfma_f32_16x16x32_bf16 v[88:91], v[220:223], v[208:211], v[88:91]
	v_mfma_f32_16x16x32_bf16 v[92:95], v[220:223], v[212:215], v[92:95]
	global_load_dwordx4 v[172:175], v57, s[8:9] offset:320
	v_mfma_f32_16x16x32_bf16 v[96:99], v[224:227], v[200:203], v[96:99]
	v_mfma_f32_16x16x32_bf16 v[100:103], v[224:227], v[204:207], v[100:103]
	global_load_dwordx4 v[176:179], v58, s[8:9] offset:0
	v_mfma_f32_16x16x32_bf16 v[104:107], v[224:227], v[208:211], v[104:107]
	v_mfma_f32_16x16x32_bf16 v[108:111], v[224:227], v[212:215], v[108:111]
	global_load_dwordx4 v[180:183], v58, s[8:9] offset:64
	v_mfma_f32_16x16x32_bf16 v[112:115], v[228:231], v[200:203], v[112:115]
	v_mfma_f32_16x16x32_bf16 v[116:119], v[228:231], v[204:207], v[116:119]
	global_load_dwordx4 v[184:187], v58, s[8:9] offset:128
	v_mfma_f32_16x16x32_bf16 v[120:123], v[228:231], v[208:211], v[120:123]
	v_mfma_f32_16x16x32_bf16 v[124:127], v[228:231], v[212:215], v[124:127]
	global_load_dwordx4 v[188:191], v58, s[8:9] offset:192
	v_mfma_f32_16x16x32_bf16 v[128:131], v[232:235], v[200:203], v[128:131]
	v_mfma_f32_16x16x32_bf16 v[132:135], v[232:235], v[204:207], v[132:135]
	global_load_dwordx4 v[192:195], v58, s[8:9] offset:256
	v_mfma_f32_16x16x32_bf16 v[136:139], v[232:235], v[208:211], v[136:139]
	v_mfma_f32_16x16x32_bf16 v[140:143], v[232:235], v[212:215], v[140:143]
	global_load_dwordx4 v[196:199], v58, s[8:9] offset:320
	v_mfma_f32_16x16x32_bf16 v[144:147], v[236:239], v[200:203], v[144:147]
	v_mfma_f32_16x16x32_bf16 v[148:151], v[236:239], v[204:207], v[148:151]
	v_mfma_f32_16x16x32_bf16 v[152:155], v[236:239], v[208:211], v[152:155]
	v_mfma_f32_16x16x32_bf16 v[156:159], v[236:239], v[212:215], v[156:159]
	v_and_b32_e32 v12, 63, v0
	v_cmp_gt_u32_e32 vcc, 16, v12
	v_xor_b32_e32 v13, 16, v12
	v_lshlrev_b32_e32 v13, 2, v13
	v_xor_b32_e32 v12, 32, v12
	v_lshlrev_b32_e32 v12, 2, v12
	v_bfe_u32 v14, v0, 6, 1
	v_mul_u32_u24_e32 v14, 0x60, v14
	v_bfe_u32 v15, v0, 4, 2
	v_lshl_add_u32 v14, v15, 2, v14
	v_add_u32_e32 v14, s13, v14
	v_lshlrev_b32_e32 v14, 2, v14
	global_load_dwordx4 v[200:203], v59, s[8:9] offset:0
	global_load_dwordx4 v[204:207], v59, s[8:9] offset:64
	global_load_dwordx4 v[208:211], v59, s[8:9] offset:128
	global_load_dwordx4 v[212:215], v59, s[8:9] offset:192
	global_load_dwordx4 v[216:219], v59, s[8:9] offset:256
	global_load_dwordx4 v[220:223], v59, s[8:9] offset:320
	v_lshrrev_b32_e32 v60, 1, v56
	v_lshrrev_b32_e32 v61, 1, v57
	v_lshrrev_b32_e32 v62, 1, v58
	v_lshrrev_b32_e32 v63, 1, v59
	v_bfe_u32 v8, v0, 7, 1
	v_and_b32_e32 v9, 15, v0
	v_lshl_add_u32 v8, v8, 6, v9
	v_add_u32_e32 v8, s12, v8
	v_lshlrev_b32_e32 v8, 6, v8
	v_bfe_u32 v9, v0, 6, 1
	v_lshlrev_b32_e32 v9, 1, v9
	v_add_u32_e32 v9, s30, v9
	v_lshl_add_u32 v8, v9, 2, v8
	v_add_u32_e32 v9, 0x400, v8
	v_add_u32_e32 v10, 0x400, v9
	v_add_u32_e32 v11, 0x400, v10
	s_waitcnt vmcnt(23)
	v_pk_add_f32 v[64:65], v[64:65], v[16:17]
	v_pk_add_f32 v[66:67], v[66:67], v[18:19]
	global_store_dwordx4 v56, v[64:67], s[10:11]
	v_pk_mul_f32 v[224:225], v[240:241], v[64:65]
	v_pk_mul_f32 v[226:227], v[242:243], v[66:67]
	v_cvt_pk_bf16_f32 v228, v224, v225
	v_cvt_pk_bf16_f32 v229, v226, v227
	global_store_dwordx2 v60, v[228:229], s[28:29]
	v_pk_mul_f32 v[230:231], v[64:65], v[64:65]
	v_pk_mul_f32 v[232:233], v[66:67], v[66:67]
	v_add_f32_e32 v230, v230, v231
	v_add_f32_e32 v230, v232, v230
	v_add_f32_e32 v234, v233, v230
	s_waitcnt vmcnt(24)
	v_pk_add_f32 v[80:81], v[80:81], v[20:21]
	v_pk_add_f32 v[82:83], v[82:83], v[22:23]
	global_store_dwordx4 v56, v[80:83], s[10:11] offset:64
	v_pk_mul_f32 v[224:225], v[244:245], v[80:81]
	v_pk_mul_f32 v[226:227], v[246:247], v[82:83]
	v_cvt_pk_bf16_f32 v228, v224, v225
	v_cvt_pk_bf16_f32 v229, v226, v227
	global_store_dwordx2 v60, v[228:229], s[28:29] offset:32
	v_pk_mul_f32 v[230:231], v[80:81], v[80:81]
	v_pk_mul_f32 v[232:233], v[82:83], v[82:83]
	v_add_f32_e32 v230, v230, v231
	v_add_f32_e32 v230, v232, v230
	v_add_f32_e32 v230, v233, v230
	v_add_f32_e32 v234, v234, v230
	s_waitcnt vmcnt(25)
	v_pk_add_f32 v[96:97], v[96:97], v[24:25]
	v_pk_add_f32 v[98:99], v[98:99], v[26:27]
	global_store_dwordx4 v56, v[96:99], s[10:11] offset:128
	v_pk_mul_f32 v[224:225], v[248:249], v[96:97]
	v_pk_mul_f32 v[226:227], v[250:251], v[98:99]
	v_cvt_pk_bf16_f32 v228, v224, v225
	v_cvt_pk_bf16_f32 v229, v226, v227
	global_store_dwordx2 v60, v[228:229], s[28:29] offset:64
	v_pk_mul_f32 v[230:231], v[96:97], v[96:97]
	v_pk_mul_f32 v[232:233], v[98:99], v[98:99]
	v_add_f32_e32 v230, v230, v231
	v_add_f32_e32 v230, v232, v230
	v_add_f32_e32 v230, v233, v230
	v_add_f32_e32 v234, v234, v230
	s_waitcnt vmcnt(26)
	v_pk_add_f32 v[112:113], v[112:113], v[28:29]
	v_pk_add_f32 v[114:115], v[114:115], v[30:31]
	global_store_dwordx4 v56, v[112:115], s[10:11] offset:192
	v_pk_mul_f32 v[224:225], v[252:253], v[112:113]
	v_pk_mul_f32 v[226:227], v[254:255], v[114:115]
	v_cvt_pk_bf16_f32 v228, v224, v225
	v_cvt_pk_bf16_f32 v229, v226, v227
	global_store_dwordx2 v60, v[228:229], s[28:29] offset:96
	v_pk_mul_f32 v[230:231], v[112:113], v[112:113]
	v_pk_mul_f32 v[232:233], v[114:115], v[114:115]
	v_add_f32_e32 v230, v230, v231
	v_add_f32_e32 v230, v232, v230
	v_add_f32_e32 v235, v233, v230
	s_waitcnt vmcnt(27)
	v_pk_add_f32 v[128:129], v[128:129], v[32:33]
	v_pk_add_f32 v[130:131], v[130:131], v[34:35]
	global_store_dwordx4 v56, v[128:131], s[10:11] offset:256
	v_pk_mul_f32 v[224:225], v[48:49], v[128:129]
	v_pk_mul_f32 v[226:227], v[50:51], v[130:131]
	v_cvt_pk_bf16_f32 v228, v224, v225
	v_cvt_pk_bf16_f32 v229, v226, v227
	global_store_dwordx2 v60, v[228:229], s[28:29] offset:128
	v_pk_mul_f32 v[230:231], v[128:129], v[128:129]
	v_pk_mul_f32 v[232:233], v[130:131], v[130:131]
	v_add_f32_e32 v230, v230, v231
	v_add_f32_e32 v230, v232, v230
	v_add_f32_e32 v230, v233, v230
	v_add_f32_e32 v235, v235, v230
	s_waitcnt vmcnt(28)
	v_pk_add_f32 v[144:145], v[144:145], v[36:37]
	v_pk_add_f32 v[146:147], v[146:147], v[38:39]
	global_store_dwordx4 v56, v[144:147], s[10:11] offset:320
	v_pk_mul_f32 v[224:225], v[52:53], v[144:145]
	v_pk_mul_f32 v[226:227], v[54:55], v[146:147]
	v_cvt_pk_bf16_f32 v228, v224, v225
	v_cvt_pk_bf16_f32 v229, v226, v227
	global_store_dwordx2 v60, v[228:229], s[28:29] offset:160
	v_pk_mul_f32 v[230:231], v[144:145], v[144:145]
	v_pk_mul_f32 v[232:233], v[146:147], v[146:147]
	v_add_f32_e32 v230, v230, v231
	v_add_f32_e32 v230, v232, v230
	v_add_f32_e32 v230, v233, v230
	v_add_f32_e32 v235, v235, v230
	s_waitcnt vmcnt(29)
	v_pk_add_f32 v[68:69], v[68:69], v[40:41]
	v_pk_add_f32 v[70:71], v[70:71], v[42:43]
	global_store_dwordx4 v57, v[68:71], s[10:11]
	v_pk_mul_f32 v[224:225], v[240:241], v[68:69]
	v_pk_mul_f32 v[226:227], v[242:243], v[70:71]
	v_cvt_pk_bf16_f32 v228, v224, v225
	v_cvt_pk_bf16_f32 v229, v226, v227
	global_store_dwordx2 v61, v[228:229], s[28:29]
	v_pk_mul_f32 v[230:231], v[68:69], v[68:69]
	v_pk_mul_f32 v[232:233], v[70:71], v[70:71]
	v_add_f32_e32 v230, v230, v231
	v_add_f32_e32 v230, v232, v230
	v_add_f32_e32 v236, v233, v230
	s_waitcnt vmcnt(30)
	v_pk_add_f32 v[84:85], v[84:85], v[44:45]
	v_pk_add_f32 v[86:87], v[86:87], v[46:47]
	global_store_dwordx4 v57, v[84:87], s[10:11] offset:64
	v_pk_mul_f32 v[224:225], v[244:245], v[84:85]
	v_pk_mul_f32 v[226:227], v[246:247], v[86:87]
	v_cvt_pk_bf16_f32 v228, v224, v225
	v_cvt_pk_bf16_f32 v229, v226, v227
	global_store_dwordx2 v61, v[228:229], s[28:29] offset:32
	v_pk_mul_f32 v[230:231], v[84:85], v[84:85]
	v_pk_mul_f32 v[232:233], v[86:87], v[86:87]
	v_add_f32_e32 v230, v230, v231
	v_add_f32_e32 v230, v232, v230
	v_add_f32_e32 v230, v233, v230
	v_add_f32_e32 v236, v236, v230
	s_waitcnt vmcnt(31)
	v_pk_add_f32 v[100:101], v[100:101], v[160:161]
	v_pk_add_f32 v[102:103], v[102:103], v[162:163]
	global_store_dwordx4 v57, v[100:103], s[10:11] offset:128
	v_pk_mul_f32 v[224:225], v[248:249], v[100:101]
	v_pk_mul_f32 v[226:227], v[250:251], v[102:103]
	v_cvt_pk_bf16_f32 v228, v224, v225
	v_cvt_pk_bf16_f32 v229, v226, v227
	global_store_dwordx2 v61, v[228:229], s[28:29] offset:64
	v_pk_mul_f32 v[230:231], v[100:101], v[100:101]
	v_pk_mul_f32 v[232:233], v[102:103], v[102:103]
	v_add_f32_e32 v230, v230, v231
	v_add_f32_e32 v230, v232, v230
	v_add_f32_e32 v230, v233, v230
	v_add_f32_e32 v236, v236, v230
	s_waitcnt vmcnt(32)
	v_pk_add_f32 v[116:117], v[116:117], v[164:165]
	v_pk_add_f32 v[118:119], v[118:119], v[166:167]
	global_store_dwordx4 v57, v[116:119], s[10:11] offset:192
	v_pk_mul_f32 v[224:225], v[252:253], v[116:117]
	v_pk_mul_f32 v[226:227], v[254:255], v[118:119]
	v_cvt_pk_bf16_f32 v228, v224, v225
	v_cvt_pk_bf16_f32 v229, v226, v227
	global_store_dwordx2 v61, v[228:229], s[28:29] offset:96
	v_pk_mul_f32 v[230:231], v[116:117], v[116:117]
	v_pk_mul_f32 v[232:233], v[118:119], v[118:119]
	v_add_f32_e32 v230, v230, v231
	v_add_f32_e32 v230, v232, v230
	v_add_f32_e32 v237, v233, v230
	s_waitcnt vmcnt(33)
	v_pk_add_f32 v[132:133], v[132:133], v[168:169]
	v_pk_add_f32 v[134:135], v[134:135], v[170:171]
	global_store_dwordx4 v57, v[132:135], s[10:11] offset:256
	v_pk_mul_f32 v[224:225], v[48:49], v[132:133]
	v_pk_mul_f32 v[226:227], v[50:51], v[134:135]
	v_cvt_pk_bf16_f32 v228, v224, v225
	v_cvt_pk_bf16_f32 v229, v226, v227
	global_store_dwordx2 v61, v[228:229], s[28:29] offset:128
	v_pk_mul_f32 v[230:231], v[132:133], v[132:133]
	v_pk_mul_f32 v[232:233], v[134:135], v[134:135]
	v_add_f32_e32 v230, v230, v231
	v_add_f32_e32 v230, v232, v230
	v_add_f32_e32 v230, v233, v230
	v_add_f32_e32 v237, v237, v230
	s_waitcnt vmcnt(34)
	v_pk_add_f32 v[148:149], v[148:149], v[172:173]
	v_pk_add_f32 v[150:151], v[150:151], v[174:175]
	global_store_dwordx4 v57, v[148:151], s[10:11] offset:320
	v_pk_mul_f32 v[224:225], v[52:53], v[148:149]
	v_pk_mul_f32 v[226:227], v[54:55], v[150:151]
	v_cvt_pk_bf16_f32 v228, v224, v225
	v_cvt_pk_bf16_f32 v229, v226, v227
	global_store_dwordx2 v61, v[228:229], s[28:29] offset:160
	v_pk_mul_f32 v[230:231], v[148:149], v[148:149]
	v_pk_mul_f32 v[232:233], v[150:151], v[150:151]
	v_add_f32_e32 v230, v230, v231
	v_add_f32_e32 v230, v232, v230
	v_add_f32_e32 v230, v233, v230
	v_add_f32_e32 v237, v237, v230
	s_waitcnt vmcnt(35)
	v_pk_add_f32 v[72:73], v[72:73], v[176:177]
	v_pk_add_f32 v[74:75], v[74:75], v[178:179]
	global_store_dwordx4 v58, v[72:75], s[10:11]
	v_pk_mul_f32 v[224:225], v[240:241], v[72:73]
	v_pk_mul_f32 v[226:227], v[242:243], v[74:75]
	v_cvt_pk_bf16_f32 v228, v224, v225
	v_cvt_pk_bf16_f32 v229, v226, v227
	global_store_dwordx2 v62, v[228:229], s[28:29]
	v_pk_mul_f32 v[230:231], v[72:73], v[72:73]
	v_pk_mul_f32 v[232:233], v[74:75], v[74:75]
	v_add_f32_e32 v230, v230, v231
	v_add_f32_e32 v230, v232, v230
	v_add_f32_e32 v238, v233, v230
	s_waitcnt vmcnt(36)
	v_pk_add_f32 v[88:89], v[88:89], v[180:181]
	v_pk_add_f32 v[90:91], v[90:91], v[182:183]
	global_store_dwordx4 v58, v[88:91], s[10:11] offset:64
	v_pk_mul_f32 v[224:225], v[244:245], v[88:89]
	v_pk_mul_f32 v[226:227], v[246:247], v[90:91]
	v_cvt_pk_bf16_f32 v228, v224, v225
	v_cvt_pk_bf16_f32 v229, v226, v227
	global_store_dwordx2 v62, v[228:229], s[28:29] offset:32
	v_pk_mul_f32 v[230:231], v[88:89], v[88:89]
	v_pk_mul_f32 v[232:233], v[90:91], v[90:91]
	v_add_f32_e32 v230, v230, v231
	v_add_f32_e32 v230, v232, v230
	v_add_f32_e32 v230, v233, v230
	v_add_f32_e32 v238, v238, v230
	s_waitcnt vmcnt(37)
	v_pk_add_f32 v[104:105], v[104:105], v[184:185]
	v_pk_add_f32 v[106:107], v[106:107], v[186:187]
	global_store_dwordx4 v58, v[104:107], s[10:11] offset:128
	v_pk_mul_f32 v[224:225], v[248:249], v[104:105]
	v_pk_mul_f32 v[226:227], v[250:251], v[106:107]
	v_cvt_pk_bf16_f32 v228, v224, v225
	v_cvt_pk_bf16_f32 v229, v226, v227
	global_store_dwordx2 v62, v[228:229], s[28:29] offset:64
	v_pk_mul_f32 v[230:231], v[104:105], v[104:105]
	v_pk_mul_f32 v[232:233], v[106:107], v[106:107]
	v_add_f32_e32 v230, v230, v231
	v_add_f32_e32 v230, v232, v230
	v_add_f32_e32 v230, v233, v230
	v_add_f32_e32 v238, v238, v230
	s_waitcnt vmcnt(38)
	v_pk_add_f32 v[120:121], v[120:121], v[188:189]
	v_pk_add_f32 v[122:123], v[122:123], v[190:191]
	global_store_dwordx4 v58, v[120:123], s[10:11] offset:192
	v_pk_mul_f32 v[224:225], v[252:253], v[120:121]
	v_pk_mul_f32 v[226:227], v[254:255], v[122:123]
	v_cvt_pk_bf16_f32 v228, v224, v225
	v_cvt_pk_bf16_f32 v229, v226, v227
	global_store_dwordx2 v62, v[228:229], s[28:29] offset:96
	v_pk_mul_f32 v[230:231], v[120:121], v[120:121]
	v_pk_mul_f32 v[232:233], v[122:123], v[122:123]
	v_add_f32_e32 v230, v230, v231
	v_add_f32_e32 v230, v232, v230
	v_add_f32_e32 v239, v233, v230
	s_waitcnt vmcnt(39)
	v_pk_add_f32 v[136:137], v[136:137], v[192:193]
	v_pk_add_f32 v[138:139], v[138:139], v[194:195]
	global_store_dwordx4 v58, v[136:139], s[10:11] offset:256
	v_pk_mul_f32 v[224:225], v[48:49], v[136:137]
	v_pk_mul_f32 v[226:227], v[50:51], v[138:139]
	v_cvt_pk_bf16_f32 v228, v224, v225
	v_cvt_pk_bf16_f32 v229, v226, v227
	global_store_dwordx2 v62, v[228:229], s[28:29] offset:128
	v_pk_mul_f32 v[230:231], v[136:137], v[136:137]
	v_pk_mul_f32 v[232:233], v[138:139], v[138:139]
	v_add_f32_e32 v230, v230, v231
	v_add_f32_e32 v230, v232, v230
	v_add_f32_e32 v230, v233, v230
	v_add_f32_e32 v239, v239, v230
	s_waitcnt vmcnt(40)
	v_pk_add_f32 v[152:153], v[152:153], v[196:197]
	v_pk_add_f32 v[154:155], v[154:155], v[198:199]
	global_store_dwordx4 v58, v[152:155], s[10:11] offset:320
	v_pk_mul_f32 v[224:225], v[52:53], v[152:153]
	v_pk_mul_f32 v[226:227], v[54:55], v[154:155]
	v_cvt_pk_bf16_f32 v228, v224, v225
	v_cvt_pk_bf16_f32 v229, v226, v227
	global_store_dwordx2 v62, v[228:229], s[28:29] offset:160
	v_pk_mul_f32 v[230:231], v[152:153], v[152:153]
	v_pk_mul_f32 v[232:233], v[154:155], v[154:155]
	v_add_f32_e32 v230, v230, v231
	v_add_f32_e32 v230, v232, v230
	v_add_f32_e32 v230, v233, v230
	v_add_f32_e32 v239, v239, v230
	s_waitcnt vmcnt(41)
	v_pk_add_f32 v[76:77], v[76:77], v[200:201]
	v_pk_add_f32 v[78:79], v[78:79], v[202:203]
	global_store_dwordx4 v59, v[76:79], s[10:11]
	v_pk_mul_f32 v[224:225], v[240:241], v[76:77]
	v_pk_mul_f32 v[226:227], v[242:243], v[78:79]
	v_cvt_pk_bf16_f32 v228, v224, v225
	v_cvt_pk_bf16_f32 v229, v226, v227
	global_store_dwordx2 v63, v[228:229], s[28:29]
	v_pk_mul_f32 v[230:231], v[76:77], v[76:77]
	v_pk_mul_f32 v[232:233], v[78:79], v[78:79]
	v_add_f32_e32 v230, v230, v231
	v_add_f32_e32 v230, v232, v230
	v_add_f32_e32 v14, v233, v230
	s_waitcnt vmcnt(42)
	v_pk_add_f32 v[92:93], v[92:93], v[204:205]
	v_pk_add_f32 v[94:95], v[94:95], v[206:207]
	global_store_dwordx4 v59, v[92:95], s[10:11] offset:64
	v_pk_mul_f32 v[224:225], v[244:245], v[92:93]
	v_pk_mul_f32 v[226:227], v[246:247], v[94:95]
	v_cvt_pk_bf16_f32 v228, v224, v225
	v_cvt_pk_bf16_f32 v229, v226, v227
	global_store_dwordx2 v63, v[228:229], s[28:29] offset:32
	v_pk_mul_f32 v[230:231], v[92:93], v[92:93]
	v_pk_mul_f32 v[232:233], v[94:95], v[94:95]
	v_add_f32_e32 v230, v230, v231
	v_add_f32_e32 v230, v232, v230
	v_add_f32_e32 v230, v233, v230
	v_add_f32_e32 v14, v14, v230
	s_waitcnt vmcnt(43)
	v_pk_add_f32 v[108:109], v[108:109], v[208:209]
	v_pk_add_f32 v[110:111], v[110:111], v[210:211]
	global_store_dwordx4 v59, v[108:111], s[10:11] offset:128
	v_pk_mul_f32 v[224:225], v[248:249], v[108:109]
	v_pk_mul_f32 v[226:227], v[250:251], v[110:111]
	v_cvt_pk_bf16_f32 v228, v224, v225
	v_cvt_pk_bf16_f32 v229, v226, v227
	global_store_dwordx2 v63, v[228:229], s[28:29] offset:64
	v_pk_mul_f32 v[230:231], v[108:109], v[108:109]
	v_pk_mul_f32 v[232:233], v[110:111], v[110:111]
	v_add_f32_e32 v230, v230, v231
	v_add_f32_e32 v230, v232, v230
	v_add_f32_e32 v230, v233, v230
	v_add_f32_e32 v14, v14, v230
	s_waitcnt vmcnt(44)
	v_pk_add_f32 v[124:125], v[124:125], v[212:213]
	v_pk_add_f32 v[126:127], v[126:127], v[214:215]
	global_store_dwordx4 v59, v[124:127], s[10:11] offset:192
	v_pk_mul_f32 v[224:225], v[252:253], v[124:125]
	v_pk_mul_f32 v[226:227], v[254:255], v[126:127]
	v_cvt_pk_bf16_f32 v228, v224, v225
	v_cvt_pk_bf16_f32 v229, v226, v227
	global_store_dwordx2 v63, v[228:229], s[28:29] offset:96
	v_pk_mul_f32 v[230:231], v[124:125], v[124:125]
	v_pk_mul_f32 v[232:233], v[126:127], v[126:127]
	v_add_f32_e32 v230, v230, v231
	v_add_f32_e32 v230, v232, v230
	v_add_f32_e32 v15, v233, v230
	s_waitcnt vmcnt(45)
	v_pk_add_f32 v[140:141], v[140:141], v[216:217]
	v_pk_add_f32 v[142:143], v[142:143], v[218:219]
	global_store_dwordx4 v59, v[140:143], s[10:11] offset:256
	v_pk_mul_f32 v[224:225], v[48:49], v[140:141]
	v_pk_mul_f32 v[226:227], v[50:51], v[142:143]
	v_cvt_pk_bf16_f32 v228, v224, v225
	v_cvt_pk_bf16_f32 v229, v226, v227
	global_store_dwordx2 v63, v[228:229], s[28:29] offset:128
	v_pk_mul_f32 v[230:231], v[140:141], v[140:141]
	v_pk_mul_f32 v[232:233], v[142:143], v[142:143]
	v_add_f32_e32 v230, v230, v231
	v_add_f32_e32 v230, v232, v230
	v_add_f32_e32 v230, v233, v230
	v_add_f32_e32 v15, v15, v230
	s_waitcnt vmcnt(46)
	v_pk_add_f32 v[156:157], v[156:157], v[220:221]
	v_pk_add_f32 v[158:159], v[158:159], v[222:223]
	global_store_dwordx4 v59, v[156:159], s[10:11] offset:320
	v_pk_mul_f32 v[224:225], v[52:53], v[156:157]
	v_pk_mul_f32 v[226:227], v[54:55], v[158:159]
	v_cvt_pk_bf16_f32 v228, v224, v225
	v_cvt_pk_bf16_f32 v229, v226, v227
	global_store_dwordx2 v63, v[228:229], s[28:29] offset:160
	v_pk_mul_f32 v[230:231], v[156:157], v[156:157]
	v_pk_mul_f32 v[232:233], v[158:159], v[158:159]
	v_add_f32_e32 v230, v230, v231
	v_add_f32_e32 v230, v232, v230
	v_add_f32_e32 v230, v233, v230
	v_add_f32_e32 v15, v15, v230
	ds_bpermute_b32 v224, v13, v234
	ds_bpermute_b32 v225, v13, v235
	ds_bpermute_b32 v226, v13, v236
	ds_bpermute_b32 v227, v13, v237
	ds_bpermute_b32 v228, v13, v238
	ds_bpermute_b32 v229, v13, v239
	ds_bpermute_b32 v230, v13, v14
	ds_bpermute_b32 v231, v13, v15
	s_waitcnt lgkmcnt(0)
	v_add_f32_e32 v234, v234, v224
	v_add_f32_e32 v235, v235, v225
	v_add_f32_e32 v236, v236, v226
	v_add_f32_e32 v237, v237, v227
	v_add_f32_e32 v238, v238, v228
	v_add_f32_e32 v239, v239, v229
	v_add_f32_e32 v14, v14, v230
	v_add_f32_e32 v15, v15, v231
	ds_bpermute_b32 v224, v12, v234
	ds_bpermute_b32 v225, v12, v235
	ds_bpermute_b32 v226, v12, v236
	ds_bpermute_b32 v227, v12, v237
	ds_bpermute_b32 v228, v12, v238
	ds_bpermute_b32 v229, v12, v239
	ds_bpermute_b32 v230, v12, v14
	ds_bpermute_b32 v231, v12, v15
	s_waitcnt lgkmcnt(0)
	v_add_f32_e32 v234, v234, v224
	v_add_f32_e32 v235, v235, v225
	v_add_f32_e32 v236, v236, v226
	v_add_f32_e32 v237, v237, v227
	v_add_f32_e32 v238, v238, v228
	v_add_f32_e32 v239, v239, v229
	v_add_f32_e32 v14, v14, v230
	v_add_f32_e32 v15, v15, v231
	s_and_saveexec_b64 s[2:3], vcc
	global_store_dwordx2 v8, v[234:235], s[26:27]
	global_store_dwordx2 v9, v[236:237], s[26:27]
	global_store_dwordx2 v10, v[238:239], s[26:27]
	global_store_dwordx2 v11, v[14:15], s[26:27]
	s_or_b64 exec, exec, s[2:3]

.Lup_loop:
	s_waitcnt lgkmcnt(0)
	v_mfma_f32_16x16x32_bf16 v[128:131], v[48:51], v[32:35], v[128:131]
	ds_read_b128 v[80:83], v13 offset:0
	v_mfma_f32_16x16x32_bf16 v[132:135], v[48:51], v[36:39], v[132:135]
	ds_read_b128 v[84:87], v13 offset:2048
	v_mfma_f32_16x16x32_bf16 v[136:139], v[48:51], v[40:43], v[136:139]
	ds_read_b128 v[88:91], v13 offset:4096
	v_mfma_f32_16x16x32_bf16 v[140:143], v[48:51], v[44:47], v[140:143]
	ds_read_b128 v[92:95], v13 offset:6144
	v_mfma_f32_16x16x32_bf16 v[144:147], v[52:55], v[32:35], v[144:147]
	ds_read_b128 v[96:99], v15 offset:0
	v_mfma_f32_16x16x32_bf16 v[148:151], v[52:55], v[36:39], v[148:151]
	ds_read_b128 v[100:103], v15 offset:2048
	v_mfma_f32_16x16x32_bf16 v[152:155], v[52:55], v[40:43], v[152:155]
	ds_read_b128 v[104:107], v15 offset:4096
	v_mfma_f32_16x16x32_bf16 v[156:159], v[52:55], v[44:47], v[156:159]
	ds_read_b128 v[108:111], v15 offset:6144
	v_mfma_f32_16x16x32_bf16 v[160:163], v[56:59], v[32:35], v[160:163]
	ds_read_b128 v[112:115], v15 offset:8192
	v_mfma_f32_16x16x32_bf16 v[164:167], v[56:59], v[36:39], v[164:167]
	ds_read_b128 v[116:119], v15 offset:10240
	v_mfma_f32_16x16x32_bf16 v[168:171], v[56:59], v[40:43], v[168:171]
	ds_read_b128 v[120:123], v15 offset:12288
	v_mfma_f32_16x16x32_bf16 v[172:175], v[56:59], v[44:47], v[172:175]
	ds_read_b128 v[124:127], v15 offset:14336
	v_mfma_f32_16x16x32_bf16 v[176:179], v[60:63], v[32:35], v[176:179]
	s_add_u32 m0, s20, 0x6000
	v_mfma_f32_16x16x32_bf16 v[180:183], v[60:63], v[36:39], v[180:183]
	global_load_lds_dwordx4 v4, s[18:19]
	v_mfma_f32_16x16x32_bf16 v[184:187], v[60:63], v[40:43], v[184:187]
	s_add_u32 m0, s20, 0x7000
	v_mfma_f32_16x16x32_bf16 v[188:191], v[60:63], v[44:47], v[188:191]
	global_load_lds_dwordx4 v5, s[18:19]
	v_mfma_f32_16x16x32_bf16 v[192:195], v[64:67], v[32:35], v[192:195]
	s_add_u32 m0, s20, 0x8000
	v_mfma_f32_16x16x32_bf16 v[196:199], v[64:67], v[36:39], v[196:199]
	global_load_lds_dwordx4 v6, s[18:19]
	v_mfma_f32_16x16x32_bf16 v[200:203], v[64:67], v[40:43], v[200:203]
	s_add_u32 m0, s20, 0x9000
	v_mfma_f32_16x16x32_bf16 v[204:207], v[64:67], v[44:47], v[204:207]
	global_load_lds_dwordx4 v7, s[18:19]
	v_mfma_f32_16x16x32_bf16 v[208:211], v[68:71], v[32:35], v[208:211]
	s_add_u32 m0, s20, 0xa000
	v_mfma_f32_16x16x32_bf16 v[212:215], v[68:71], v[36:39], v[212:215]
	global_load_lds_dwordx4 v8, s[18:19]
	v_mfma_f32_16x16x32_bf16 v[216:219], v[68:71], v[40:43], v[216:219]
	s_add_u32 m0, s20, 0xb000
	v_mfma_f32_16x16x32_bf16 v[220:223], v[68:71], v[44:47], v[220:223]
	global_load_lds_dwordx4 v9, s[18:19]
	v_mfma_f32_16x16x32_bf16 v[224:227], v[72:75], v[32:35], v[224:227]
	v_mfma_f32_16x16x32_bf16 v[228:231], v[72:75], v[36:39], v[228:231]
	v_mfma_f32_16x16x32_bf16 v[232:235], v[72:75], v[40:43], v[232:235]
	v_mfma_f32_16x16x32_bf16 v[236:239], v[72:75], v[44:47], v[236:239]
	v_mfma_f32_16x16x32_bf16 v[240:243], v[76:79], v[32:35], v[240:243]
	s_add_u32 s16, s16, 0x80
	s_addc_u32 s17, s17, 0
	s_add_u32 s18, s18, 0x80
	s_addc_u32 s19, s19, 0
	v_mfma_f32_16x16x32_bf16 v[244:247], v[76:79], v[36:39], v[244:247]
	s_add_u32 s20, s20, 0xc000
	s_sub_u32 s22, s20, 0x24000
	s_cmp_ge_u32 s20, 0x24000
	s_cselect_b32 s20, s22, s20
	v_mfma_f32_16x16x32_bf16 v[248:251], v[76:79], v[40:43], v[248:251]
	v_add_u32_e32 v12, s21, v10
	v_add_u32_e32 v14, s21, v11
	v_xor_b32_e32 v13, 64, v12
	v_xor_b32_e32 v15, 64, v14
	v_mfma_f32_16x16x32_bf16 v[252:255], v[76:79], v[44:47], v[252:255]
	s_add_u32 s21, s21, 0xc000
	s_sub_u32 s23, s21, 0x24000
	s_cmp_ge_u32 s21, 0x24000
	s_cselect_b32 s21, s23, s21
	s_waitcnt lgkmcnt(0)
	v_mfma_f32_16x16x32_bf16 v[128:131], v[96:99], v[80:83], v[128:131]
	v_mfma_f32_16x16x32_bf16 v[132:135], v[96:99], v[84:87], v[132:135]
	v_mfma_f32_16x16x32_bf16 v[136:139], v[96:99], v[88:91], v[136:139]
	v_mfma_f32_16x16x32_bf16 v[140:143], v[96:99], v[92:95], v[140:143]
	v_mfma_f32_16x16x32_bf16 v[144:147], v[100:103], v[80:83], v[144:147]
	v_mfma_f32_16x16x32_bf16 v[148:151], v[100:103], v[84:87], v[148:151]
	v_mfma_f32_16x16x32_bf16 v[152:155], v[100:103], v[88:91], v[152:155]
	v_mfma_f32_16x16x32_bf16 v[156:159], v[100:103], v[92:95], v[156:159]
	s_waitcnt vmcnt(12)
	s_barrier
	v_mfma_f32_16x16x32_bf16 v[160:163], v[104:107], v[80:83], v[160:163]
	ds_read_b128 v[32:35], v12 offset:0
	v_mfma_f32_16x16x32_bf16 v[164:167], v[104:107], v[84:87], v[164:167]
	ds_read_b128 v[36:39], v12 offset:2048
	v_mfma_f32_16x16x32_bf16 v[168:171], v[104:107], v[88:91], v[168:171]
	ds_read_b128 v[40:43], v12 offset:4096
	v_mfma_f32_16x16x32_bf16 v[172:175], v[104:107], v[92:95], v[172:175]
	ds_read_b128 v[44:47], v12 offset:6144
	v_mfma_f32_16x16x32_bf16 v[176:179], v[108:111], v[80:83], v[176:179]
	ds_read_b128 v[48:51], v14 offset:0
	v_mfma_f32_16x16x32_bf16 v[180:183], v[108:111], v[84:87], v[180:183]
	ds_read_b128 v[52:55], v14 offset:2048
	v_mfma_f32_16x16x32_bf16 v[184:187], v[108:111], v[88:91], v[184:187]
	ds_read_b128 v[56:59], v14 offset:4096
	v_mfma_f32_16x16x32_bf16 v[188:191], v[108:111], v[92:95], v[188:191]
	ds_read_b128 v[60:63], v14 offset:6144
	v_mfma_f32_16x16x32_bf16 v[192:195], v[112:115], v[80:83], v[192:195]
	ds_read_b128 v[64:67], v14 offset:8192
	v_mfma_f32_16x16x32_bf16 v[196:199], v[112:115], v[84:87], v[196:199]
	ds_read_b128 v[68:71], v14 offset:10240
	v_mfma_f32_16x16x32_bf16 v[200:203], v[112:115], v[88:91], v[200:203]
	ds_read_b128 v[72:75], v14 offset:12288
	v_mfma_f32_16x16x32_bf16 v[204:207], v[112:115], v[92:95], v[204:207]
	ds_read_b128 v[76:79], v14 offset:14336
	v_mfma_f32_16x16x32_bf16 v[208:211], v[116:119], v[80:83], v[208:211]
	s_add_u32 m0, s20, 0x0
	v_mfma_f32_16x16x32_bf16 v[212:215], v[116:119], v[84:87], v[212:215]
	global_load_lds_dwordx4 v2, s[16:17]
	v_mfma_f32_16x16x32_bf16 v[216:219], v[116:119], v[88:91], v[216:219]
	s_add_u32 m0, s20, 0x1000
	v_mfma_f32_16x16x32_bf16 v[220:223], v[116:119], v[92:95], v[220:223]
	global_load_lds_dwordx4 v3, s[16:17]
	v_mfma_f32_16x16x32_bf16 v[224:227], v[120:123], v[80:83], v[224:227]
	s_add_u32 m0, s20, 0x2000
	v_mfma_f32_16x16x32_bf16 v[228:231], v[120:123], v[84:87], v[228:231]
	global_load_lds_dwordx4 v4, s[16:17]
	v_mfma_f32_16x16x32_bf16 v[232:235], v[120:123], v[88:91], v[232:235]
	s_add_u32 m0, s20, 0x3000
	v_mfma_f32_16x16x32_bf16 v[236:239], v[120:123], v[92:95], v[236:239]
	global_load_lds_dwordx4 v5, s[16:17]
	v_mfma_f32_16x16x32_bf16 v[240:243], v[124:127], v[80:83], v[240:243]
	s_add_u32 m0, s20, 0x4000
	v_mfma_f32_16x16x32_bf16 v[244:247], v[124:127], v[84:87], v[244:247]
	global_load_lds_dwordx4 v2, s[18:19]
	v_mfma_f32_16x16x32_bf16 v[248:251], v[124:127], v[88:91], v[248:251]
	s_add_u32 m0, s20, 0x5000
	v_mfma_f32_16x16x32_bf16 v[252:255], v[124:127], v[92:95], v[252:255]
	global_load_lds_dwordx4 v3, s[18:19]
	s_add_u32 s15, s15, 1
	s_cmp_lt_u32 s15, 9
	s_cbranch_scc1 .Lup_loop
	s_waitcnt lgkmcnt(0)
	v_mfma_f32_16x16x32_bf16 v[128:131], v[48:51], v[32:35], v[128:131]
	ds_read_b128 v[80:83], v13 offset:0
	v_mfma_f32_16x16x32_bf16 v[132:135], v[48:51], v[36:39], v[132:135]
	ds_read_b128 v[84:87], v13 offset:2048
	v_mfma_f32_16x16x32_bf16 v[136:139], v[48:51], v[40:43], v[136:139]
	ds_read_b128 v[88:91], v13 offset:4096
	v_mfma_f32_16x16x32_bf16 v[140:143], v[48:51], v[44:47], v[140:143]
	ds_read_b128 v[92:95], v13 offset:6144
	v_mfma_f32_16x16x32_bf16 v[144:147], v[52:55], v[32:35], v[144:147]
	ds_read_b128 v[96:99], v15 offset:0
	v_mfma_f32_16x16x32_bf16 v[148:151], v[52:55], v[36:39], v[148:151]
	ds_read_b128 v[100:103], v15 offset:2048
	v_mfma_f32_16x16x32_bf16 v[152:155], v[52:55], v[40:43], v[152:155]
	ds_read_b128 v[104:107], v15 offset:4096
	v_mfma_f32_16x16x32_bf16 v[156:159], v[52:55], v[44:47], v[156:159]
	ds_read_b128 v[108:111], v15 offset:6144
	v_mfma_f32_16x16x32_bf16 v[160:163], v[56:59], v[32:35], v[160:163]
	ds_read_b128 v[112:115], v15 offset:8192
	v_mfma_f32_16x16x32_bf16 v[164:167], v[56:59], v[36:39], v[164:167]
	ds_read_b128 v[116:119], v15 offset:10240
	v_mfma_f32_16x16x32_bf16 v[168:171], v[56:59], v[40:43], v[168:171]
	ds_read_b128 v[120:123], v15 offset:12288
	v_mfma_f32_16x16x32_bf16 v[172:175], v[56:59], v[44:47], v[172:175]
	ds_read_b128 v[124:127], v15 offset:14336
	v_mfma_f32_16x16x32_bf16 v[176:179], v[60:63], v[32:35], v[176:179]
	s_add_u32 m0, s20, 0x6000
	v_mfma_f32_16x16x32_bf16 v[180:183], v[60:63], v[36:39], v[180:183]
	global_load_lds_dwordx4 v4, s[18:19]
	v_mfma_f32_16x16x32_bf16 v[184:187], v[60:63], v[40:43], v[184:187]
	s_add_u32 m0, s20, 0x7000
	v_mfma_f32_16x16x32_bf16 v[188:191], v[60:63], v[44:47], v[188:191]
	global_load_lds_dwordx4 v5, s[18:19]
	v_mfma_f32_16x16x32_bf16 v[192:195], v[64:67], v[32:35], v[192:195]
	s_add_u32 m0, s20, 0x8000
	v_mfma_f32_16x16x32_bf16 v[196:199], v[64:67], v[36:39], v[196:199]
	global_load_lds_dwordx4 v6, s[18:19]
	v_mfma_f32_16x16x32_bf16 v[200:203], v[64:67], v[40:43], v[200:203]
	s_add_u32 m0, s20, 0x9000
	v_mfma_f32_16x16x32_bf16 v[204:207], v[64:67], v[44:47], v[204:207]
	global_load_lds_dwordx4 v7, s[18:19]
	v_mfma_f32_16x16x32_bf16 v[208:211], v[68:71], v[32:35], v[208:211]
	s_add_u32 m0, s20, 0xa000
	v_mfma_f32_16x16x32_bf16 v[212:215], v[68:71], v[36:39], v[212:215]
	global_load_lds_dwordx4 v8, s[18:19]
	v_mfma_f32_16x16x32_bf16 v[216:219], v[68:71], v[40:43], v[216:219]
	s_add_u32 m0, s20, 0xb000
	v_mfma_f32_16x16x32_bf16 v[220:223], v[68:71], v[44:47], v[220:223]
	global_load_lds_dwordx4 v9, s[18:19]
	v_mfma_f32_16x16x32_bf16 v[224:227], v[72:75], v[32:35], v[224:227]
	v_mfma_f32_16x16x32_bf16 v[228:231], v[72:75], v[36:39], v[228:231]
	v_mfma_f32_16x16x32_bf16 v[232:235], v[72:75], v[40:43], v[232:235]
	v_mfma_f32_16x16x32_bf16 v[236:239], v[72:75], v[44:47], v[236:239]
	v_mfma_f32_16x16x32_bf16 v[240:243], v[76:79], v[32:35], v[240:243]
	s_add_u32 s16, s16, 0x80
	s_addc_u32 s17, s17, 0
	s_add_u32 s18, s18, 0x80
	s_addc_u32 s19, s19, 0
	v_mfma_f32_16x16x32_bf16 v[244:247], v[76:79], v[36:39], v[244:247]
	s_add_u32 s20, s20, 0xc000
	s_sub_u32 s22, s20, 0x24000
	s_cmp_ge_u32 s20, 0x24000
	s_cselect_b32 s20, s22, s20
	v_mfma_f32_16x16x32_bf16 v[248:251], v[76:79], v[40:43], v[248:251]
	v_add_u32_e32 v12, s21, v10
	v_add_u32_e32 v14, s21, v11
	v_xor_b32_e32 v13, 64, v12
	v_xor_b32_e32 v15, 64, v14
	v_mfma_f32_16x16x32_bf16 v[252:255], v[76:79], v[44:47], v[252:255]
	s_add_u32 s21, s21, 0xc000
	s_sub_u32 s23, s21, 0x24000
	s_cmp_ge_u32 s21, 0x24000
	s_cselect_b32 s21, s23, s21
	s_waitcnt lgkmcnt(0)
	v_mfma_f32_16x16x32_bf16 v[128:131], v[96:99], v[80:83], v[128:131]
	v_mfma_f32_16x16x32_bf16 v[132:135], v[96:99], v[84:87], v[132:135]
	v_mfma_f32_16x16x32_bf16 v[136:139], v[96:99], v[88:91], v[136:139]
	v_mfma_f32_16x16x32_bf16 v[140:143], v[96:99], v[92:95], v[140:143]
	v_mfma_f32_16x16x32_bf16 v[144:147], v[100:103], v[80:83], v[144:147]
	v_mfma_f32_16x16x32_bf16 v[148:151], v[100:103], v[84:87], v[148:151]
	v_mfma_f32_16x16x32_bf16 v[152:155], v[100:103], v[88:91], v[152:155]
	v_mfma_f32_16x16x32_bf16 v[156:159], v[100:103], v[92:95], v[156:159]
	s_waitcnt vmcnt(12)
	s_barrier
	v_mfma_f32_16x16x32_bf16 v[160:163], v[104:107], v[80:83], v[160:163]
	ds_read_b128 v[32:35], v12 offset:0
	v_mfma_f32_16x16x32_bf16 v[164:167], v[104:107], v[84:87], v[164:167]
	ds_read_b128 v[36:39], v12 offset:2048
	v_mfma_f32_16x16x32_bf16 v[168:171], v[104:107], v[88:91], v[168:171]
	ds_read_b128 v[40:43], v12 offset:4096
	v_mfma_f32_16x16x32_bf16 v[172:175], v[104:107], v[92:95], v[172:175]
	ds_read_b128 v[44:47], v12 offset:6144
	v_mfma_f32_16x16x32_bf16 v[176:179], v[108:111], v[80:83], v[176:179]
	ds_read_b128 v[48:51], v14 offset:0
	v_mfma_f32_16x16x32_bf16 v[180:183], v[108:111], v[84:87], v[180:183]
	ds_read_b128 v[52:55], v14 offset:2048
	v_mfma_f32_16x16x32_bf16 v[184:187], v[108:111], v[88:91], v[184:187]
	ds_read_b128 v[56:59], v14 offset:4096
	v_mfma_f32_16x16x32_bf16 v[188:191], v[108:111], v[92:95], v[188:191]
	ds_read_b128 v[60:63], v14 offset:6144
	v_mfma_f32_16x16x32_bf16 v[192:195], v[112:115], v[80:83], v[192:195]
	ds_read_b128 v[64:67], v14 offset:8192
	v_mfma_f32_16x16x32_bf16 v[196:199], v[112:115], v[84:87], v[196:199]
	ds_read_b128 v[68:71], v14 offset:10240
	v_mfma_f32_16x16x32_bf16 v[200:203], v[112:115], v[88:91], v[200:203]
	ds_read_b128 v[72:75], v14 offset:12288
	v_mfma_f32_16x16x32_bf16 v[204:207], v[112:115], v[92:95], v[204:207]
	ds_read_b128 v[76:79], v14 offset:14336
	v_mfma_f32_16x16x32_bf16 v[208:211], v[116:119], v[80:83], v[208:211]
	v_mfma_f32_16x16x32_bf16 v[212:215], v[116:119], v[84:87], v[212:215]
	v_mfma_f32_16x16x32_bf16 v[216:219], v[116:119], v[88:91], v[216:219]
	v_mfma_f32_16x16x32_bf16 v[220:223], v[116:119], v[92:95], v[220:223]
	v_mfma_f32_16x16x32_bf16 v[224:227], v[120:123], v[80:83], v[224:227]
	v_mfma_f32_16x16x32_bf16 v[228:231], v[120:123], v[84:87], v[228:231]
	v_mfma_f32_16x16x32_bf16 v[232:235], v[120:123], v[88:91], v[232:235]
	v_mfma_f32_16x16x32_bf16 v[236:239], v[120:123], v[92:95], v[236:239]
	v_mfma_f32_16x16x32_bf16 v[240:243], v[124:127], v[80:83], v[240:243]
	v_mfma_f32_16x16x32_bf16 v[244:247], v[124:127], v[84:87], v[244:247]
	v_mfma_f32_16x16x32_bf16 v[248:251], v[124:127], v[88:91], v[248:251]
	v_mfma_f32_16x16x32_bf16 v[252:255], v[124:127], v[92:95], v[252:255]
	s_waitcnt lgkmcnt(0)
	v_mfma_f32_16x16x32_bf16 v[128:131], v[48:51], v[32:35], v[128:131]
	ds_read_b128 v[80:83], v13 offset:0
	v_mfma_f32_16x16x32_bf16 v[132:135], v[48:51], v[36:39], v[132:135]
	ds_read_b128 v[84:87], v13 offset:2048
	v_mfma_f32_16x16x32_bf16 v[136:139], v[48:51], v[40:43], v[136:139]
	ds_read_b128 v[88:91], v13 offset:4096
	v_mfma_f32_16x16x32_bf16 v[140:143], v[48:51], v[44:47], v[140:143]
	ds_read_b128 v[92:95], v13 offset:6144
	v_mfma_f32_16x16x32_bf16 v[144:147], v[52:55], v[32:35], v[144:147]
	ds_read_b128 v[96:99], v15 offset:0
	v_mfma_f32_16x16x32_bf16 v[148:151], v[52:55], v[36:39], v[148:151]
	ds_read_b128 v[100:103], v15 offset:2048
	v_mfma_f32_16x16x32_bf16 v[152:155], v[52:55], v[40:43], v[152:155]
	ds_read_b128 v[104:107], v15 offset:4096
	v_mfma_f32_16x16x32_bf16 v[156:159], v[52:55], v[44:47], v[156:159]
	ds_read_b128 v[108:111], v15 offset:6144
	v_mfma_f32_16x16x32_bf16 v[160:163], v[56:59], v[32:35], v[160:163]
	ds_read_b128 v[112:115], v15 offset:8192
	v_mfma_f32_16x16x32_bf16 v[164:167], v[56:59], v[36:39], v[164:167]
	ds_read_b128 v[116:119], v15 offset:10240
	v_mfma_f32_16x16x32_bf16 v[168:171], v[56:59], v[40:43], v[168:171]
	ds_read_b128 v[120:123], v15 offset:12288
	v_mfma_f32_16x16x32_bf16 v[172:175], v[56:59], v[44:47], v[172:175]
	ds_read_b128 v[124:127], v15 offset:14336
	v_mfma_f32_16x16x32_bf16 v[176:179], v[60:63], v[32:35], v[176:179]
	v_mfma_f32_16x16x32_bf16 v[180:183], v[60:63], v[36:39], v[180:183]
	v_mfma_f32_16x16x32_bf16 v[184:187], v[60:63], v[40:43], v[184:187]
	v_mfma_f32_16x16x32_bf16 v[188:191], v[60:63], v[44:47], v[188:191]
	v_mfma_f32_16x16x32_bf16 v[192:195], v[64:67], v[32:35], v[192:195]
	v_mfma_f32_16x16x32_bf16 v[196:199], v[64:67], v[36:39], v[196:199]
	v_mfma_f32_16x16x32_bf16 v[200:203], v[64:67], v[40:43], v[200:203]
	v_mfma_f32_16x16x32_bf16 v[204:207], v[64:67], v[44:47], v[204:207]
	v_mfma_f32_16x16x32_bf16 v[208:211], v[68:71], v[32:35], v[208:211]
	v_mfma_f32_16x16x32_bf16 v[212:215], v[68:71], v[36:39], v[212:215]
	v_mfma_f32_16x16x32_bf16 v[216:219], v[68:71], v[40:43], v[216:219]
	v_mfma_f32_16x16x32_bf16 v[220:223], v[68:71], v[44:47], v[220:223]
	v_mfma_f32_16x16x32_bf16 v[224:227], v[72:75], v[32:35], v[224:227]
	v_mfma_f32_16x16x32_bf16 v[228:231], v[72:75], v[36:39], v[228:231]
	v_mfma_f32_16x16x32_bf16 v[232:235], v[72:75], v[40:43], v[232:235]
	v_mfma_f32_16x16x32_bf16 v[236:239], v[72:75], v[44:47], v[236:239]
	v_mfma_f32_16x16x32_bf16 v[240:243], v[76:79], v[32:35], v[240:243]
	v_add_u32_e32 v12, s21, v10
	v_add_u32_e32 v14, s21, v11
	v_xor_b32_e32 v13, 64, v12
	v_xor_b32_e32 v15, 64, v14
	v_mfma_f32_16x16x32_bf16 v[244:247], v[76:79], v[36:39], v[244:247]
	s_add_u32 s21, s21, 0xc000
	s_sub_u32 s23, s21, 0x24000
	s_cmp_ge_u32 s21, 0x24000
	s_cselect_b32 s21, s23, s21
	v_mfma_f32_16x16x32_bf16 v[248:251], v[76:79], v[40:43], v[248:251]
	v_mfma_f32_16x16x32_bf16 v[252:255], v[76:79], v[44:47], v[252:255]
	s_waitcnt lgkmcnt(0)
	v_mfma_f32_16x16x32_bf16 v[128:131], v[96:99], v[80:83], v[128:131]
	v_mfma_f32_16x16x32_bf16 v[132:135], v[96:99], v[84:87], v[132:135]
	v_mfma_f32_16x16x32_bf16 v[136:139], v[96:99], v[88:91], v[136:139]
	v_mfma_f32_16x16x32_bf16 v[140:143], v[96:99], v[92:95], v[140:143]
	v_mfma_f32_16x16x32_bf16 v[144:147], v[100:103], v[80:83], v[144:147]
	v_mfma_f32_16x16x32_bf16 v[148:151], v[100:103], v[84:87], v[148:151]
	v_mfma_f32_16x16x32_bf16 v[152:155], v[100:103], v[88:91], v[152:155]
	v_mfma_f32_16x16x32_bf16 v[156:159], v[100:103], v[92:95], v[156:159]
	s_waitcnt vmcnt(0)
	s_barrier
	v_mfma_f32_16x16x32_bf16 v[160:163], v[104:107], v[80:83], v[160:163]
	ds_read_b128 v[32:35], v12 offset:0
	v_mfma_f32_16x16x32_bf16 v[164:167], v[104:107], v[84:87], v[164:167]
	ds_read_b128 v[36:39], v12 offset:2048
	v_mfma_f32_16x16x32_bf16 v[168:171], v[104:107], v[88:91], v[168:171]
	ds_read_b128 v[40:43], v12 offset:4096
	v_mfma_f32_16x16x32_bf16 v[172:175], v[104:107], v[92:95], v[172:175]
	ds_read_b128 v[44:47], v12 offset:6144
	v_mfma_f32_16x16x32_bf16 v[176:179], v[108:111], v[80:83], v[176:179]
	ds_read_b128 v[48:51], v14 offset:0
	v_mfma_f32_16x16x32_bf16 v[180:183], v[108:111], v[84:87], v[180:183]
	ds_read_b128 v[52:55], v14 offset:2048
	v_mfma_f32_16x16x32_bf16 v[184:187], v[108:111], v[88:91], v[184:187]
	ds_read_b128 v[56:59], v14 offset:4096
	v_mfma_f32_16x16x32_bf16 v[188:191], v[108:111], v[92:95], v[188:191]
	ds_read_b128 v[60:63], v14 offset:6144
	v_mfma_f32_16x16x32_bf16 v[192:195], v[112:115], v[80:83], v[192:195]
	ds_read_b128 v[64:67], v14 offset:8192
	v_mfma_f32_16x16x32_bf16 v[196:199], v[112:115], v[84:87], v[196:199]
	ds_read_b128 v[68:71], v14 offset:10240
	v_mfma_f32_16x16x32_bf16 v[200:203], v[112:115], v[88:91], v[200:203]
	ds_read_b128 v[72:75], v14 offset:12288
	v_mfma_f32_16x16x32_bf16 v[204:207], v[112:115], v[92:95], v[204:207]
	ds_read_b128 v[76:79], v14 offset:14336
	v_mfma_f32_16x16x32_bf16 v[208:211], v[116:119], v[80:83], v[208:211]
	v_mfma_f32_16x16x32_bf16 v[212:215], v[116:119], v[84:87], v[212:215]
	v_mfma_f32_16x16x32_bf16 v[216:219], v[116:119], v[88:91], v[216:219]
	v_mfma_f32_16x16x32_bf16 v[220:223], v[116:119], v[92:95], v[220:223]
	v_mfma_f32_16x16x32_bf16 v[224:227], v[120:123], v[80:83], v[224:227]
	v_mfma_f32_16x16x32_bf16 v[228:231], v[120:123], v[84:87], v[228:231]
	v_mfma_f32_16x16x32_bf16 v[232:235], v[120:123], v[88:91], v[232:235]
	v_mfma_f32_16x16x32_bf16 v[236:239], v[120:123], v[92:95], v[236:239]
	v_mfma_f32_16x16x32_bf16 v[240:243], v[124:127], v[80:83], v[240:243]
	v_mfma_f32_16x16x32_bf16 v[244:247], v[124:127], v[84:87], v[244:247]
	v_mfma_f32_16x16x32_bf16 v[248:251], v[124:127], v[88:91], v[248:251]
	v_mfma_f32_16x16x32_bf16 v[252:255], v[124:127], v[92:95], v[252:255]
	s_waitcnt lgkmcnt(0)
	v_mfma_f32_16x16x32_bf16 v[128:131], v[48:51], v[32:35], v[128:131]
	ds_read_b128 v[80:83], v13 offset:0
	v_mfma_f32_16x16x32_bf16 v[132:135], v[48:51], v[36:39], v[132:135]
	ds_read_b128 v[84:87], v13 offset:2048
	v_mfma_f32_16x16x32_bf16 v[136:139], v[48:51], v[40:43], v[136:139]
	ds_read_b128 v[88:91], v13 offset:4096
	v_mfma_f32_16x16x32_bf16 v[140:143], v[48:51], v[44:47], v[140:143]
	ds_read_b128 v[92:95], v13 offset:6144
	v_mfma_f32_16x16x32_bf16 v[144:147], v[52:55], v[32:35], v[144:147]
	ds_read_b128 v[96:99], v15 offset:0
	v_mfma_f32_16x16x32_bf16 v[148:151], v[52:55], v[36:39], v[148:151]
	ds_read_b128 v[100:103], v15 offset:2048
	v_mfma_f32_16x16x32_bf16 v[152:155], v[52:55], v[40:43], v[152:155]
	ds_read_b128 v[104:107], v15 offset:4096
	v_mfma_f32_16x16x32_bf16 v[156:159], v[52:55], v[44:47], v[156:159]
	ds_read_b128 v[108:111], v15 offset:6144
	v_mfma_f32_16x16x32_bf16 v[160:163], v[56:59], v[32:35], v[160:163]
	ds_read_b128 v[112:115], v15 offset:8192
	v_mfma_f32_16x16x32_bf16 v[164:167], v[56:59], v[36:39], v[164:167]
	ds_read_b128 v[116:119], v15 offset:10240
	v_mfma_f32_16x16x32_bf16 v[168:171], v[56:59], v[40:43], v[168:171]
	ds_read_b128 v[120:123], v15 offset:12288
	v_mfma_f32_16x16x32_bf16 v[172:175], v[56:59], v[44:47], v[172:175]
	ds_read_b128 v[124:127], v15 offset:14336
	v_mfma_f32_16x16x32_bf16 v[176:179], v[60:63], v[32:35], v[176:179]
	v_mfma_f32_16x16x32_bf16 v[180:183], v[60:63], v[36:39], v[180:183]
	v_mfma_f32_16x16x32_bf16 v[184:187], v[60:63], v[40:43], v[184:187]
	v_mfma_f32_16x16x32_bf16 v[188:191], v[60:63], v[44:47], v[188:191]
	v_mfma_f32_16x16x32_bf16 v[192:195], v[64:67], v[32:35], v[192:195]
	v_mfma_f32_16x16x32_bf16 v[196:199], v[64:67], v[36:39], v[196:199]
	v_mfma_f32_16x16x32_bf16 v[200:203], v[64:67], v[40:43], v[200:203]
	v_mfma_f32_16x16x32_bf16 v[204:207], v[64:67], v[44:47], v[204:207]
	v_mfma_f32_16x16x32_bf16 v[208:211], v[68:71], v[32:35], v[208:211]
	v_mfma_f32_16x16x32_bf16 v[212:215], v[68:71], v[36:39], v[212:215]
	v_mfma_f32_16x16x32_bf16 v[216:219], v[68:71], v[40:43], v[216:219]
	v_mfma_f32_16x16x32_bf16 v[220:223], v[68:71], v[44:47], v[220:223]
	v_mfma_f32_16x16x32_bf16 v[224:227], v[72:75], v[32:35], v[224:227]
	v_mfma_f32_16x16x32_bf16 v[228:231], v[72:75], v[36:39], v[228:231]
	v_mfma_f32_16x16x32_bf16 v[232:235], v[72:75], v[40:43], v[232:235]
	v_mfma_f32_16x16x32_bf16 v[236:239], v[72:75], v[44:47], v[236:239]
	v_mfma_f32_16x16x32_bf16 v[240:243], v[76:79], v[32:35], v[240:243]
	v_mfma_f32_16x16x32_bf16 v[244:247], v[76:79], v[36:39], v[244:247]
	v_mfma_f32_16x16x32_bf16 v[248:251], v[76:79], v[40:43], v[248:251]
	v_mfma_f32_16x16x32_bf16 v[252:255], v[76:79], v[44:47], v[252:255]
	s_waitcnt lgkmcnt(0)
	v_mfma_f32_16x16x32_bf16 v[128:131], v[96:99], v[80:83], v[128:131]
	v_mfma_f32_16x16x32_bf16 v[132:135], v[96:99], v[84:87], v[132:135]
	global_load_dwordx4 v[32:35], v21, s[8:9] offset:0
	v_mfma_f32_16x16x32_bf16 v[136:139], v[96:99], v[88:91], v[136:139]
	v_mfma_f32_16x16x32_bf16 v[140:143], v[96:99], v[92:95], v[140:143]
	global_load_dwordx4 v[36:39], v21, s[8:9] offset:16
	v_mfma_f32_16x16x32_bf16 v[144:147], v[100:103], v[80:83], v[144:147]
	v_mfma_f32_16x16x32_bf16 v[148:151], v[100:103], v[84:87], v[148:151]
	global_load_dwordx4 v[40:43], v21, s[8:9] offset:32
	v_mfma_f32_16x16x32_bf16 v[152:155], v[100:103], v[88:91], v[152:155]
	v_mfma_f32_16x16x32_bf16 v[156:159], v[100:103], v[92:95], v[156:159]
	global_load_dwordx4 v[44:47], v21, s[8:9] offset:48
	v_mfma_f32_16x16x32_bf16 v[160:163], v[104:107], v[80:83], v[160:163]
	v_mfma_f32_16x16x32_bf16 v[164:167], v[104:107], v[84:87], v[164:167]
	global_load_dwordx4 v[48:51], v21, s[8:9] offset:1024
	v_mfma_f32_16x16x32_bf16 v[168:171], v[104:107], v[88:91], v[168:171]
	v_mfma_f32_16x16x32_bf16 v[172:175], v[104:107], v[92:95], v[172:175]
	global_load_dwordx4 v[52:55], v21, s[8:9] offset:1040
	v_mfma_f32_16x16x32_bf16 v[176:179], v[108:111], v[80:83], v[176:179]
	v_mfma_f32_16x16x32_bf16 v[180:183], v[108:111], v[84:87], v[180:183]
	global_load_dwordx4 v[56:59], v21, s[8:9] offset:1056
	v_mfma_f32_16x16x32_bf16 v[184:187], v[108:111], v[88:91], v[184:187]
	v_mfma_f32_16x16x32_bf16 v[188:191], v[108:111], v[92:95], v[188:191]
	global_load_dwordx4 v[60:63], v21, s[8:9] offset:1072
	v_mfma_f32_16x16x32_bf16 v[192:195], v[112:115], v[80:83], v[192:195]
	v_mfma_f32_16x16x32_bf16 v[196:199], v[112:115], v[84:87], v[196:199]
	global_load_dwordx4 v[64:67], v21, s[8:9] offset:2048
	v_mfma_f32_16x16x32_bf16 v[200:203], v[112:115], v[88:91], v[200:203]
	v_mfma_f32_16x16x32_bf16 v[204:207], v[112:115], v[92:95], v[204:207]
	global_load_dwordx4 v[68:71], v21, s[8:9] offset:2064
	v_mfma_f32_16x16x32_bf16 v[208:211], v[116:119], v[80:83], v[208:211]
	v_mfma_f32_16x16x32_bf16 v[212:215], v[116:119], v[84:87], v[212:215]
	global_load_dwordx4 v[72:75], v21, s[8:9] offset:2080
	v_mfma_f32_16x16x32_bf16 v[216:219], v[116:119], v[88:91], v[216:219]
	v_mfma_f32_16x16x32_bf16 v[220:223], v[116:119], v[92:95], v[220:223]
	global_load_dwordx4 v[76:79], v21, s[8:9] offset:2096
	v_mfma_f32_16x16x32_bf16 v[224:227], v[120:123], v[80:83], v[224:227]
	v_mfma_f32_16x16x32_bf16 v[228:231], v[120:123], v[84:87], v[228:231]
	v_mfma_f32_16x16x32_bf16 v[232:235], v[120:123], v[88:91], v[232:235]
	v_mfma_f32_16x16x32_bf16 v[236:239], v[120:123], v[92:95], v[236:239]
	v_mfma_f32_16x16x32_bf16 v[240:243], v[124:127], v[80:83], v[240:243]
	v_mfma_f32_16x16x32_bf16 v[244:247], v[124:127], v[84:87], v[244:247]
	v_mfma_f32_16x16x32_bf16 v[248:251], v[124:127], v[88:91], v[248:251]
	v_mfma_f32_16x16x32_bf16 v[252:255], v[124:127], v[92:95], v[252:255]
	global_load_dwordx4 v[80:83], v21, s[8:9] offset:3072
	global_load_dwordx4 v[84:87], v21, s[8:9] offset:3088
	global_load_dwordx4 v[88:91], v21, s[8:9] offset:3104
	global_load_dwordx4 v[92:95], v21, s[8:9] offset:3120
	v_mov_b32_e32 v31, 0x358637bd
	s_waitcnt vmcnt(0)
	v_add_f32_e32 v32, v32, v33
	v_add_f32_e32 v34, v34, v35
	v_add_f32_e32 v36, v36, v37
	v_add_f32_e32 v38, v38, v39
	v_add_f32_e32 v40, v40, v41
	v_add_f32_e32 v42, v42, v43
	v_add_f32_e32 v44, v44, v45
	v_add_f32_e32 v46, v46, v47
	v_add_f32_e32 v32, v32, v34
	v_add_f32_e32 v36, v36, v38
	v_add_f32_e32 v40, v40, v42
	v_add_f32_e32 v44, v44, v46
	v_add_f32_e32 v32, v32, v36
	v_add_f32_e32 v40, v40, v44
	v_add_f32_e32 v32, v32, v40
	v_add_f32_e32 v48, v48, v49
	v_add_f32_e32 v50, v50, v51
	v_add_f32_e32 v52, v52, v53
	v_add_f32_e32 v54, v54, v55
	v_add_f32_e32 v56, v56, v57
	v_add_f32_e32 v58, v58, v59
	v_add_f32_e32 v60, v60, v61
	v_add_f32_e32 v62, v62, v63
	v_add_f32_e32 v48, v48, v50
	v_add_f32_e32 v52, v52, v54
	v_add_f32_e32 v56, v56, v58
	v_add_f32_e32 v60, v60, v62
	v_add_f32_e32 v48, v48, v52
	v_add_f32_e32 v56, v56, v60
	v_add_f32_e32 v48, v48, v56
	v_add_f32_e32 v64, v64, v65
	v_add_f32_e32 v66, v66, v67
	v_add_f32_e32 v68, v68, v69
	v_add_f32_e32 v70, v70, v71
	v_add_f32_e32 v72, v72, v73
	v_add_f32_e32 v74, v74, v75
	v_add_f32_e32 v76, v76, v77
	v_add_f32_e32 v78, v78, v79
	v_add_f32_e32 v64, v64, v66
	v_add_f32_e32 v68, v68, v70
	v_add_f32_e32 v72, v72, v74
	v_add_f32_e32 v76, v76, v78
	v_add_f32_e32 v64, v64, v68
	v_add_f32_e32 v72, v72, v76
	v_add_f32_e32 v64, v64, v72
	v_add_f32_e32 v80, v80, v81
	v_add_f32_e32 v82, v82, v83
	v_add_f32_e32 v84, v84, v85
	v_add_f32_e32 v86, v86, v87
	v_add_f32_e32 v88, v88, v89
	v_add_f32_e32 v90, v90, v91
	v_add_f32_e32 v92, v92, v93
	v_add_f32_e32 v94, v94, v95
	v_add_f32_e32 v80, v80, v82
	v_add_f32_e32 v84, v84, v86
	v_add_f32_e32 v88, v88, v90
	v_add_f32_e32 v92, v92, v94
	v_add_f32_e32 v80, v80, v84
	v_add_f32_e32 v88, v88, v92
	v_add_f32_e32 v80, v80, v88
	v_fmamk_f32 v20, v32, 0x3aaaaaab, v31
	v_fmamk_f32 v22, v48, 0x3aaaaaab, v31
	v_fmamk_f32 v24, v64, 0x3aaaaaab, v31
	v_fmamk_f32 v26, v80, 0x3aaaaaab, v31
	v_rsq_f32_e32 v20, v20
	v_rsq_f32_e32 v22, v22
	v_rsq_f32_e32 v24, v24
	v_rsq_f32_e32 v26, v26
	s_nop 0
	v_pk_mul_f32 v[128:129], v[128:129], v[20:21] op_sel_hi:[1,0]
	v_pk_mul_f32 v[130:131], v[130:131], v[20:21] op_sel_hi:[1,0]
	v_pk_mul_f32 v[144:145], v[144:145], v[20:21] op_sel_hi:[1,0]
	v_pk_mul_f32 v[146:147], v[146:147], v[20:21] op_sel_hi:[1,0]
	v_pk_mul_f32 v[32:33], v[128:129], s[26:27]
	v_pk_mul_f32 v[34:35], v[130:131], s[26:27]
	v_pk_mul_f32 v[36:37], v[144:145], s[26:27]
	v_pk_mul_f32 v[38:39], v[146:147], s[26:27]
	v_pk_fma_f32 v[32:33], v[128:129], v[32:33], s[28:29] neg_lo:[1,0,0] neg_hi:[1,0,0]
	v_pk_fma_f32 v[34:35], v[130:131], v[34:35], s[28:29] neg_lo:[1,0,0] neg_hi:[1,0,0]
	v_pk_fma_f32 v[36:37], v[144:145], v[36:37], s[28:29] neg_lo:[1,0,0] neg_hi:[1,0,0]
	v_pk_fma_f32 v[38:39], v[146:147], v[38:39], s[28:29] neg_lo:[1,0,0] neg_hi:[1,0,0]
	v_pk_mul_f32 v[32:33], v[128:129], v[32:33]
	v_pk_mul_f32 v[34:35], v[130:131], v[34:35]
	v_pk_mul_f32 v[36:37], v[144:145], v[36:37]
	v_pk_mul_f32 v[38:39], v[146:147], v[38:39]
	v_exp_f32_e32 v32, v32
	v_exp_f32_e32 v33, v33
	v_exp_f32_e32 v34, v34
	v_exp_f32_e32 v35, v35
	v_exp_f32_e32 v36, v36
	v_exp_f32_e32 v37, v37
	v_exp_f32_e32 v38, v38
	v_exp_f32_e32 v39, v39
	v_pk_add_f32 v[32:33], v[32:33], s[30:31]
	v_pk_add_f32 v[34:35], v[34:35], s[30:31]
	v_pk_add_f32 v[36:37], v[36:37], s[30:31]
	v_pk_add_f32 v[38:39], v[38:39], s[30:31]
	v_rcp_f32_e32 v32, v32
	v_rcp_f32_e32 v33, v33
	v_rcp_f32_e32 v34, v34
	v_rcp_f32_e32 v35, v35
	v_rcp_f32_e32 v36, v36
	v_rcp_f32_e32 v37, v37
	v_rcp_f32_e32 v38, v38
	v_rcp_f32_e32 v39, v39
	s_nop 0
	v_pk_mul_f32 v[128:129], v[128:129], v[32:33]
	v_pk_mul_f32 v[130:131], v[130:131], v[34:35]
	v_pk_mul_f32 v[144:145], v[144:145], v[36:37]
	v_pk_mul_f32 v[146:147], v[146:147], v[38:39]
	v_cvt_pk_bf16_f32 v64, v128, v129
	v_cvt_pk_bf16_f32 v65, v130, v131
	v_cvt_pk_bf16_f32 v66, v144, v145
	v_cvt_pk_bf16_f32 v67, v146, v147
	global_store_dwordx2 v16, v[64:65], s[10:11]
	global_store_dwordx2 v16, v[66:67], s[10:11] offset:32
	v_pk_mul_f32 v[160:161], v[160:161], v[20:21] op_sel_hi:[1,0]
	v_pk_mul_f32 v[162:163], v[162:163], v[20:21] op_sel_hi:[1,0]
	v_pk_mul_f32 v[176:177], v[176:177], v[20:21] op_sel_hi:[1,0]
	v_pk_mul_f32 v[178:179], v[178:179], v[20:21] op_sel_hi:[1,0]
	v_pk_mul_f32 v[48:49], v[160:161], s[26:27]
	v_pk_mul_f32 v[50:51], v[162:163], s[26:27]
	v_pk_mul_f32 v[52:53], v[176:177], s[26:27]
	v_pk_mul_f32 v[54:55], v[178:179], s[26:27]
	v_pk_fma_f32 v[48:49], v[160:161], v[48:49], s[28:29] neg_lo:[1,0,0] neg_hi:[1,0,0]
	v_pk_fma_f32 v[50:51], v[162:163], v[50:51], s[28:29] neg_lo:[1,0,0] neg_hi:[1,0,0]
	v_pk_fma_f32 v[52:53], v[176:177], v[52:53], s[28:29] neg_lo:[1,0,0] neg_hi:[1,0,0]
	v_pk_fma_f32 v[54:55], v[178:179], v[54:55], s[28:29] neg_lo:[1,0,0] neg_hi:[1,0,0]
	v_pk_mul_f32 v[48:49], v[160:161], v[48:49]
	v_pk_mul_f32 v[50:51], v[162:163], v[50:51]
	v_pk_mul_f32 v[52:53], v[176:177], v[52:53]
	v_pk_mul_f32 v[54:55], v[178:179], v[54:55]
	v_exp_f32_e32 v48, v48
	v_exp_f32_e32 v49, v49
	v_exp_f32_e32 v50, v50
	v_exp_f32_e32 v51, v51
	v_exp_f32_e32 v52, v52
	v_exp_f32_e32 v53, v53
	v_exp_f32_e32 v54, v54
	v_exp_f32_e32 v55, v55
	v_pk_add_f32 v[48:49], v[48:49], s[30:31]
	v_pk_add_f32 v[50:51], v[50:51], s[30:31]
	v_pk_add_f32 v[52:53], v[52:53], s[30:31]
	v_pk_add_f32 v[54:55], v[54:55], s[30:31]
	v_rcp_f32_e32 v48, v48
	v_rcp_f32_e32 v49, v49
	v_rcp_f32_e32 v50, v50
	v_rcp_f32_e32 v51, v51
	v_rcp_f32_e32 v52, v52
	v_rcp_f32_e32 v53, v53
	v_rcp_f32_e32 v54, v54
	v_rcp_f32_e32 v55, v55
	s_nop 0
	v_pk_mul_f32 v[160:161], v[160:161], v[48:49]
	v_pk_mul_f32 v[162:163], v[162:163], v[50:51]
	v_pk_mul_f32 v[176:177], v[176:177], v[52:53]
	v_pk_mul_f32 v[178:179], v[178:179], v[54:55]
	v_cvt_pk_bf16_f32 v68, v160, v161
	v_cvt_pk_bf16_f32 v69, v162, v163
	v_cvt_pk_bf16_f32 v70, v176, v177
	v_cvt_pk_bf16_f32 v71, v178, v179
	global_store_dwordx2 v16, v[68:69], s[10:11] offset:64
	global_store_dwordx2 v16, v[70:71], s[10:11] offset:96
	v_pk_mul_f32 v[192:193], v[192:193], v[20:21] op_sel_hi:[1,0]
	v_pk_mul_f32 v[194:195], v[194:195], v[20:21] op_sel_hi:[1,0]
	v_pk_mul_f32 v[208:209], v[208:209], v[20:21] op_sel_hi:[1,0]
	v_pk_mul_f32 v[210:211], v[210:211], v[20:21] op_sel_hi:[1,0]
	v_pk_mul_f32 v[32:33], v[192:193], s[26:27]
	v_pk_mul_f32 v[34:35], v[194:195], s[26:27]
	v_pk_mul_f32 v[36:37], v[208:209], s[26:27]
	v_pk_mul_f32 v[38:39], v[210:211], s[26:27]
	v_pk_fma_f32 v[32:33], v[192:193], v[32:33], s[28:29] neg_lo:[1,0,0] neg_hi:[1,0,0]
	v_pk_fma_f32 v[34:35], v[194:195], v[34:35], s[28:29] neg_lo:[1,0,0] neg_hi:[1,0,0]
	v_pk_fma_f32 v[36:37], v[208:209], v[36:37], s[28:29] neg_lo:[1,0,0] neg_hi:[1,0,0]
	v_pk_fma_f32 v[38:39], v[210:211], v[38:39], s[28:29] neg_lo:[1,0,0] neg_hi:[1,0,0]
	v_pk_mul_f32 v[32:33], v[192:193], v[32:33]
	v_pk_mul_f32 v[34:35], v[194:195], v[34:35]
	v_pk_mul_f32 v[36:37], v[208:209], v[36:37]
	v_pk_mul_f32 v[38:39], v[210:211], v[38:39]
	v_exp_f32_e32 v32, v32
	v_exp_f32_e32 v33, v33
	v_exp_f32_e32 v34, v34
	v_exp_f32_e32 v35, v35
	v_exp_f32_e32 v36, v36
	v_exp_f32_e32 v37, v37
	v_exp_f32_e32 v38, v38
	v_exp_f32_e32 v39, v39
	v_pk_add_f32 v[32:33], v[32:33], s[30:31]
	v_pk_add_f32 v[34:35], v[34:35], s[30:31]
	v_pk_add_f32 v[36:37], v[36:37], s[30:31]
	v_pk_add_f32 v[38:39], v[38:39], s[30:31]
	v_rcp_f32_e32 v32, v32
	v_rcp_f32_e32 v33, v33
	v_rcp_f32_e32 v34, v34
	v_rcp_f32_e32 v35, v35
	v_rcp_f32_e32 v36, v36
	v_rcp_f32_e32 v37, v37
	v_rcp_f32_e32 v38, v38
	v_rcp_f32_e32 v39, v39
	s_nop 0
	v_pk_mul_f32 v[192:193], v[192:193], v[32:33]
	v_pk_mul_f32 v[194:195], v[194:195], v[34:35]
	v_pk_mul_f32 v[208:209], v[208:209], v[36:37]
	v_pk_mul_f32 v[210:211], v[210:211], v[38:39]
	v_cvt_pk_bf16_f32 v64, v192, v193
	v_cvt_pk_bf16_f32 v65, v194, v195
	v_cvt_pk_bf16_f32 v66, v208, v209
	v_cvt_pk_bf16_f32 v67, v210, v211
	global_store_dwordx2 v16, v[64:65], s[10:11] offset:128
	global_store_dwordx2 v16, v[66:67], s[10:11] offset:160
	v_pk_mul_f32 v[224:225], v[224:225], v[20:21] op_sel_hi:[1,0]
	v_pk_mul_f32 v[226:227], v[226:227], v[20:21] op_sel_hi:[1,0]
	v_pk_mul_f32 v[240:241], v[240:241], v[20:21] op_sel_hi:[1,0]
	v_pk_mul_f32 v[242:243], v[242:243], v[20:21] op_sel_hi:[1,0]
	v_pk_mul_f32 v[48:49], v[224:225], s[26:27]
	v_pk_mul_f32 v[50:51], v[226:227], s[26:27]
	v_pk_mul_f32 v[52:53], v[240:241], s[26:27]
	v_pk_mul_f32 v[54:55], v[242:243], s[26:27]
	v_pk_fma_f32 v[48:49], v[224:225], v[48:49], s[28:29] neg_lo:[1,0,0] neg_hi:[1,0,0]
	v_pk_fma_f32 v[50:51], v[226:227], v[50:51], s[28:29] neg_lo:[1,0,0] neg_hi:[1,0,0]
	v_pk_fma_f32 v[52:53], v[240:241], v[52:53], s[28:29] neg_lo:[1,0,0] neg_hi:[1,0,0]
	v_pk_fma_f32 v[54:55], v[242:243], v[54:55], s[28:29] neg_lo:[1,0,0] neg_hi:[1,0,0]
	v_pk_mul_f32 v[48:49], v[224:225], v[48:49]
	v_pk_mul_f32 v[50:51], v[226:227], v[50:51]
	v_pk_mul_f32 v[52:53], v[240:241], v[52:53]
	v_pk_mul_f32 v[54:55], v[242:243], v[54:55]
	v_exp_f32_e32 v48, v48
	v_exp_f32_e32 v49, v49
	v_exp_f32_e32 v50, v50
	v_exp_f32_e32 v51, v51
	v_exp_f32_e32 v52, v52
	v_exp_f32_e32 v53, v53
	v_exp_f32_e32 v54, v54
	v_exp_f32_e32 v55, v55
	v_pk_add_f32 v[48:49], v[48:49], s[30:31]
	v_pk_add_f32 v[50:51], v[50:51], s[30:31]
	v_pk_add_f32 v[52:53], v[52:53], s[30:31]
	v_pk_add_f32 v[54:55], v[54:55], s[30:31]
	v_rcp_f32_e32 v48, v48
	v_rcp_f32_e32 v49, v49
	v_rcp_f32_e32 v50, v50
	v_rcp_f32_e32 v51, v51
	v_rcp_f32_e32 v52, v52
	v_rcp_f32_e32 v53, v53
	v_rcp_f32_e32 v54, v54
	v_rcp_f32_e32 v55, v55
	s_nop 0
	v_pk_mul_f32 v[224:225], v[224:225], v[48:49]
	v_pk_mul_f32 v[226:227], v[226:227], v[50:51]
	v_pk_mul_f32 v[240:241], v[240:241], v[52:53]
	v_pk_mul_f32 v[242:243], v[242:243], v[54:55]
	v_cvt_pk_bf16_f32 v68, v224, v225
	v_cvt_pk_bf16_f32 v69, v226, v227
	v_cvt_pk_bf16_f32 v70, v240, v241
	v_cvt_pk_bf16_f32 v71, v242, v243
	global_store_dwordx2 v16, v[68:69], s[10:11] offset:192
	global_store_dwordx2 v16, v[70:71], s[10:11] offset:224
	v_pk_mul_f32 v[132:133], v[132:133], v[22:23] op_sel_hi:[1,0]
	v_pk_mul_f32 v[134:135], v[134:135], v[22:23] op_sel_hi:[1,0]
	v_pk_mul_f32 v[148:149], v[148:149], v[22:23] op_sel_hi:[1,0]
	v_pk_mul_f32 v[150:151], v[150:151], v[22:23] op_sel_hi:[1,0]
	v_pk_mul_f32 v[32:33], v[132:133], s[26:27]
	v_pk_mul_f32 v[34:35], v[134:135], s[26:27]
	v_pk_mul_f32 v[36:37], v[148:149], s[26:27]
	v_pk_mul_f32 v[38:39], v[150:151], s[26:27]
	v_pk_fma_f32 v[32:33], v[132:133], v[32:33], s[28:29] neg_lo:[1,0,0] neg_hi:[1,0,0]
	v_pk_fma_f32 v[34:35], v[134:135], v[34:35], s[28:29] neg_lo:[1,0,0] neg_hi:[1,0,0]
	v_pk_fma_f32 v[36:37], v[148:149], v[36:37], s[28:29] neg_lo:[1,0,0] neg_hi:[1,0,0]
	v_pk_fma_f32 v[38:39], v[150:151], v[38:39], s[28:29] neg_lo:[1,0,0] neg_hi:[1,0,0]
	v_pk_mul_f32 v[32:33], v[132:133], v[32:33]
	v_pk_mul_f32 v[34:35], v[134:135], v[34:35]
	v_pk_mul_f32 v[36:37], v[148:149], v[36:37]
	v_pk_mul_f32 v[38:39], v[150:151], v[38:39]
	v_exp_f32_e32 v32, v32
	v_exp_f32_e32 v33, v33
	v_exp_f32_e32 v34, v34
	v_exp_f32_e32 v35, v35
	v_exp_f32_e32 v36, v36
	v_exp_f32_e32 v37, v37
	v_exp_f32_e32 v38, v38
	v_exp_f32_e32 v39, v39
	v_pk_add_f32 v[32:33], v[32:33], s[30:31]
	v_pk_add_f32 v[34:35], v[34:35], s[30:31]
	v_pk_add_f32 v[36:37], v[36:37], s[30:31]
	v_pk_add_f32 v[38:39], v[38:39], s[30:31]
	v_rcp_f32_e32 v32, v32
	v_rcp_f32_e32 v33, v33
	v_rcp_f32_e32 v34, v34
	v_rcp_f32_e32 v35, v35
	v_rcp_f32_e32 v36, v36
	v_rcp_f32_e32 v37, v37
	v_rcp_f32_e32 v38, v38
	v_rcp_f32_e32 v39, v39
	s_nop 0
	v_pk_mul_f32 v[132:133], v[132:133], v[32:33]
	v_pk_mul_f32 v[134:135], v[134:135], v[34:35]
	v_pk_mul_f32 v[148:149], v[148:149], v[36:37]
	v_pk_mul_f32 v[150:151], v[150:151], v[38:39]
	v_cvt_pk_bf16_f32 v64, v132, v133
	v_cvt_pk_bf16_f32 v65, v134, v135
	v_cvt_pk_bf16_f32 v66, v148, v149
	v_cvt_pk_bf16_f32 v67, v150, v151
	global_store_dwordx2 v17, v[64:65], s[10:11]
	global_store_dwordx2 v17, v[66:67], s[10:11] offset:32
	v_pk_mul_f32 v[164:165], v[164:165], v[22:23] op_sel_hi:[1,0]
	v_pk_mul_f32 v[166:167], v[166:167], v[22:23] op_sel_hi:[1,0]
	v_pk_mul_f32 v[180:181], v[180:181], v[22:23] op_sel_hi:[1,0]
	v_pk_mul_f32 v[182:183], v[182:183], v[22:23] op_sel_hi:[1,0]
	v_pk_mul_f32 v[48:49], v[164:165], s[26:27]
	v_pk_mul_f32 v[50:51], v[166:167], s[26:27]
	v_pk_mul_f32 v[52:53], v[180:181], s[26:27]
	v_pk_mul_f32 v[54:55], v[182:183], s[26:27]
	v_pk_fma_f32 v[48:49], v[164:165], v[48:49], s[28:29] neg_lo:[1,0,0] neg_hi:[1,0,0]
	v_pk_fma_f32 v[50:51], v[166:167], v[50:51], s[28:29] neg_lo:[1,0,0] neg_hi:[1,0,0]
	v_pk_fma_f32 v[52:53], v[180:181], v[52:53], s[28:29] neg_lo:[1,0,0] neg_hi:[1,0,0]
	v_pk_fma_f32 v[54:55], v[182:183], v[54:55], s[28:29] neg_lo:[1,0,0] neg_hi:[1,0,0]
	v_pk_mul_f32 v[48:49], v[164:165], v[48:49]
	v_pk_mul_f32 v[50:51], v[166:167], v[50:51]
	v_pk_mul_f32 v[52:53], v[180:181], v[52:53]
	v_pk_mul_f32 v[54:55], v[182:183], v[54:55]
	v_exp_f32_e32 v48, v48
	v_exp_f32_e32 v49, v49
	v_exp_f32_e32 v50, v50
	v_exp_f32_e32 v51, v51
	v_exp_f32_e32 v52, v52
	v_exp_f32_e32 v53, v53
	v_exp_f32_e32 v54, v54
	v_exp_f32_e32 v55, v55
	v_pk_add_f32 v[48:49], v[48:49], s[30:31]
	v_pk_add_f32 v[50:51], v[50:51], s[30:31]
	v_pk_add_f32 v[52:53], v[52:53], s[30:31]
	v_pk_add_f32 v[54:55], v[54:55], s[30:31]
	v_rcp_f32_e32 v48, v48
	v_rcp_f32_e32 v49, v49
	v_rcp_f32_e32 v50, v50
	v_rcp_f32_e32 v51, v51
	v_rcp_f32_e32 v52, v52
	v_rcp_f32_e32 v53, v53
	v_rcp_f32_e32 v54, v54
	v_rcp_f32_e32 v55, v55
	s_nop 0
	v_pk_mul_f32 v[164:165], v[164:165], v[48:49]
	v_pk_mul_f32 v[166:167], v[166:167], v[50:51]
	v_pk_mul_f32 v[180:181], v[180:181], v[52:53]
	v_pk_mul_f32 v[182:183], v[182:183], v[54:55]
	v_cvt_pk_bf16_f32 v68, v164, v165
	v_cvt_pk_bf16_f32 v69, v166, v167
	v_cvt_pk_bf16_f32 v70, v180, v181
	v_cvt_pk_bf16_f32 v71, v182, v183
	global_store_dwordx2 v17, v[68:69], s[10:11] offset:64
	global_store_dwordx2 v17, v[70:71], s[10:11] offset:96
	v_pk_mul_f32 v[196:197], v[196:197], v[22:23] op_sel_hi:[1,0]
	v_pk_mul_f32 v[198:199], v[198:199], v[22:23] op_sel_hi:[1,0]
	v_pk_mul_f32 v[212:213], v[212:213], v[22:23] op_sel_hi:[1,0]
	v_pk_mul_f32 v[214:215], v[214:215], v[22:23] op_sel_hi:[1,0]
	v_pk_mul_f32 v[32:33], v[196:197], s[26:27]
	v_pk_mul_f32 v[34:35], v[198:199], s[26:27]
	v_pk_mul_f32 v[36:37], v[212:213], s[26:27]
	v_pk_mul_f32 v[38:39], v[214:215], s[26:27]
	v_pk_fma_f32 v[32:33], v[196:197], v[32:33], s[28:29] neg_lo:[1,0,0] neg_hi:[1,0,0]
	v_pk_fma_f32 v[34:35], v[198:199], v[34:35], s[28:29] neg_lo:[1,0,0] neg_hi:[1,0,0]
	v_pk_fma_f32 v[36:37], v[212:213], v[36:37], s[28:29] neg_lo:[1,0,0] neg_hi:[1,0,0]
	v_pk_fma_f32 v[38:39], v[214:215], v[38:39], s[28:29] neg_lo:[1,0,0] neg_hi:[1,0,0]
	v_pk_mul_f32 v[32:33], v[196:197], v[32:33]
	v_pk_mul_f32 v[34:35], v[198:199], v[34:35]
	v_pk_mul_f32 v[36:37], v[212:213], v[36:37]
	v_pk_mul_f32 v[38:39], v[214:215], v[38:39]
	v_exp_f32_e32 v32, v32
	v_exp_f32_e32 v33, v33
	v_exp_f32_e32 v34, v34
	v_exp_f32_e32 v35, v35
	v_exp_f32_e32 v36, v36
	v_exp_f32_e32 v37, v37
	v_exp_f32_e32 v38, v38
	v_exp_f32_e32 v39, v39
	v_pk_add_f32 v[32:33], v[32:33], s[30:31]
	v_pk_add_f32 v[34:35], v[34:35], s[30:31]
	v_pk_add_f32 v[36:37], v[36:37], s[30:31]
	v_pk_add_f32 v[38:39], v[38:39], s[30:31]
	v_rcp_f32_e32 v32, v32
	v_rcp_f32_e32 v33, v33
	v_rcp_f32_e32 v34, v34
	v_rcp_f32_e32 v35, v35
	v_rcp_f32_e32 v36, v36
	v_rcp_f32_e32 v37, v37
	v_rcp_f32_e32 v38, v38
	v_rcp_f32_e32 v39, v39
	s_nop 0
	v_pk_mul_f32 v[196:197], v[196:197], v[32:33]
	v_pk_mul_f32 v[198:199], v[198:199], v[34:35]
	v_pk_mul_f32 v[212:213], v[212:213], v[36:37]
	v_pk_mul_f32 v[214:215], v[214:215], v[38:39]
	v_cvt_pk_bf16_f32 v64, v196, v197
	v_cvt_pk_bf16_f32 v65, v198, v199
	v_cvt_pk_bf16_f32 v66, v212, v213
	v_cvt_pk_bf16_f32 v67, v214, v215
	global_store_dwordx2 v17, v[64:65], s[10:11] offset:128
	global_store_dwordx2 v17, v[66:67], s[10:11] offset:160
	v_pk_mul_f32 v[228:229], v[228:229], v[22:23] op_sel_hi:[1,0]
	v_pk_mul_f32 v[230:231], v[230:231], v[22:23] op_sel_hi:[1,0]
	v_pk_mul_f32 v[244:245], v[244:245], v[22:23] op_sel_hi:[1,0]
	v_pk_mul_f32 v[246:247], v[246:247], v[22:23] op_sel_hi:[1,0]
	v_pk_mul_f32 v[48:49], v[228:229], s[26:27]
	v_pk_mul_f32 v[50:51], v[230:231], s[26:27]
	v_pk_mul_f32 v[52:53], v[244:245], s[26:27]
	v_pk_mul_f32 v[54:55], v[246:247], s[26:27]
	v_pk_fma_f32 v[48:49], v[228:229], v[48:49], s[28:29] neg_lo:[1,0,0] neg_hi:[1,0,0]
	v_pk_fma_f32 v[50:51], v[230:231], v[50:51], s[28:29] neg_lo:[1,0,0] neg_hi:[1,0,0]
	v_pk_fma_f32 v[52:53], v[244:245], v[52:53], s[28:29] neg_lo:[1,0,0] neg_hi:[1,0,0]
	v_pk_fma_f32 v[54:55], v[246:247], v[54:55], s[28:29] neg_lo:[1,0,0] neg_hi:[1,0,0]
	v_pk_mul_f32 v[48:49], v[228:229], v[48:49]
	v_pk_mul_f32 v[50:51], v[230:231], v[50:51]
	v_pk_mul_f32 v[52:53], v[244:245], v[52:53]
	v_pk_mul_f32 v[54:55], v[246:247], v[54:55]
	v_exp_f32_e32 v48, v48
	v_exp_f32_e32 v49, v49
	v_exp_f32_e32 v50, v50
	v_exp_f32_e32 v51, v51
	v_exp_f32_e32 v52, v52
	v_exp_f32_e32 v53, v53
	v_exp_f32_e32 v54, v54
	v_exp_f32_e32 v55, v55
	v_pk_add_f32 v[48:49], v[48:49], s[30:31]
	v_pk_add_f32 v[50:51], v[50:51], s[30:31]
	v_pk_add_f32 v[52:53], v[52:53], s[30:31]
	v_pk_add_f32 v[54:55], v[54:55], s[30:31]
	v_rcp_f32_e32 v48, v48
	v_rcp_f32_e32 v49, v49
	v_rcp_f32_e32 v50, v50
	v_rcp_f32_e32 v51, v51
	v_rcp_f32_e32 v52, v52
	v_rcp_f32_e32 v53, v53
	v_rcp_f32_e32 v54, v54
	v_rcp_f32_e32 v55, v55
	s_nop 0
	v_pk_mul_f32 v[228:229], v[228:229], v[48:49]
	v_pk_mul_f32 v[230:231], v[230:231], v[50:51]
	v_pk_mul_f32 v[244:245], v[244:245], v[52:53]
	v_pk_mul_f32 v[246:247], v[246:247], v[54:55]
	v_cvt_pk_bf16_f32 v68, v228, v229
	v_cvt_pk_bf16_f32 v69, v230, v231
	v_cvt_pk_bf16_f32 v70, v244, v245
	v_cvt_pk_bf16_f32 v71, v246, v247
	global_store_dwordx2 v17, v[68:69], s[10:11] offset:192
	global_store_dwordx2 v17, v[70:71], s[10:11] offset:224
	v_pk_mul_f32 v[136:137], v[136:137], v[24:25] op_sel_hi:[1,0]
	v_pk_mul_f32 v[138:139], v[138:139], v[24:25] op_sel_hi:[1,0]
	v_pk_mul_f32 v[152:153], v[152:153], v[24:25] op_sel_hi:[1,0]
	v_pk_mul_f32 v[154:155], v[154:155], v[24:25] op_sel_hi:[1,0]
	v_pk_mul_f32 v[32:33], v[136:137], s[26:27]
	v_pk_mul_f32 v[34:35], v[138:139], s[26:27]
	v_pk_mul_f32 v[36:37], v[152:153], s[26:27]
	v_pk_mul_f32 v[38:39], v[154:155], s[26:27]
	v_pk_fma_f32 v[32:33], v[136:137], v[32:33], s[28:29] neg_lo:[1,0,0] neg_hi:[1,0,0]
	v_pk_fma_f32 v[34:35], v[138:139], v[34:35], s[28:29] neg_lo:[1,0,0] neg_hi:[1,0,0]
	v_pk_fma_f32 v[36:37], v[152:153], v[36:37], s[28:29] neg_lo:[1,0,0] neg_hi:[1,0,0]
	v_pk_fma_f32 v[38:39], v[154:155], v[38:39], s[28:29] neg_lo:[1,0,0] neg_hi:[1,0,0]
	v_pk_mul_f32 v[32:33], v[136:137], v[32:33]
	v_pk_mul_f32 v[34:35], v[138:139], v[34:35]
	v_pk_mul_f32 v[36:37], v[152:153], v[36:37]
	v_pk_mul_f32 v[38:39], v[154:155], v[38:39]
	v_exp_f32_e32 v32, v32
	v_exp_f32_e32 v33, v33
	v_exp_f32_e32 v34, v34
	v_exp_f32_e32 v35, v35
	v_exp_f32_e32 v36, v36
	v_exp_f32_e32 v37, v37
	v_exp_f32_e32 v38, v38
	v_exp_f32_e32 v39, v39
	v_pk_add_f32 v[32:33], v[32:33], s[30:31]
	v_pk_add_f32 v[34:35], v[34:35], s[30:31]
	v_pk_add_f32 v[36:37], v[36:37], s[30:31]
	v_pk_add_f32 v[38:39], v[38:39], s[30:31]
	v_rcp_f32_e32 v32, v32
	v_rcp_f32_e32 v33, v33
	v_rcp_f32_e32 v34, v34
	v_rcp_f32_e32 v35, v35
	v_rcp_f32_e32 v36, v36
	v_rcp_f32_e32 v37, v37
	v_rcp_f32_e32 v38, v38
	v_rcp_f32_e32 v39, v39
	s_nop 0
	v_pk_mul_f32 v[136:137], v[136:137], v[32:33]
	v_pk_mul_f32 v[138:139], v[138:139], v[34:35]
	v_pk_mul_f32 v[152:153], v[152:153], v[36:37]
	v_pk_mul_f32 v[154:155], v[154:155], v[38:39]
	v_cvt_pk_bf16_f32 v64, v136, v137
	v_cvt_pk_bf16_f32 v65, v138, v139
	v_cvt_pk_bf16_f32 v66, v152, v153
	v_cvt_pk_bf16_f32 v67, v154, v155
	global_store_dwordx2 v18, v[64:65], s[10:11]
	global_store_dwordx2 v18, v[66:67], s[10:11] offset:32
	v_pk_mul_f32 v[168:169], v[168:169], v[24:25] op_sel_hi:[1,0]
	v_pk_mul_f32 v[170:171], v[170:171], v[24:25] op_sel_hi:[1,0]
	v_pk_mul_f32 v[184:185], v[184:185], v[24:25] op_sel_hi:[1,0]
	v_pk_mul_f32 v[186:187], v[186:187], v[24:25] op_sel_hi:[1,0]
	v_pk_mul_f32 v[48:49], v[168:169], s[26:27]
	v_pk_mul_f32 v[50:51], v[170:171], s[26:27]
	v_pk_mul_f32 v[52:53], v[184:185], s[26:27]
	v_pk_mul_f32 v[54:55], v[186:187], s[26:27]
	v_pk_fma_f32 v[48:49], v[168:169], v[48:49], s[28:29] neg_lo:[1,0,0] neg_hi:[1,0,0]
	v_pk_fma_f32 v[50:51], v[170:171], v[50:51], s[28:29] neg_lo:[1,0,0] neg_hi:[1,0,0]
	v_pk_fma_f32 v[52:53], v[184:185], v[52:53], s[28:29] neg_lo:[1,0,0] neg_hi:[1,0,0]
	v_pk_fma_f32 v[54:55], v[186:187], v[54:55], s[28:29] neg_lo:[1,0,0] neg_hi:[1,0,0]
	v_pk_mul_f32 v[48:49], v[168:169], v[48:49]
	v_pk_mul_f32 v[50:51], v[170:171], v[50:51]
	v_pk_mul_f32 v[52:53], v[184:185], v[52:53]
	v_pk_mul_f32 v[54:55], v[186:187], v[54:55]
	v_exp_f32_e32 v48, v48
	v_exp_f32_e32 v49, v49
	v_exp_f32_e32 v50, v50
	v_exp_f32_e32 v51, v51
	v_exp_f32_e32 v52, v52
	v_exp_f32_e32 v53, v53
	v_exp_f32_e32 v54, v54
	v_exp_f32_e32 v55, v55
	v_pk_add_f32 v[48:49], v[48:49], s[30:31]
	v_pk_add_f32 v[50:51], v[50:51], s[30:31]
	v_pk_add_f32 v[52:53], v[52:53], s[30:31]
	v_pk_add_f32 v[54:55], v[54:55], s[30:31]
	v_rcp_f32_e32 v48, v48
	v_rcp_f32_e32 v49, v49
	v_rcp_f32_e32 v50, v50
	v_rcp_f32_e32 v51, v51
	v_rcp_f32_e32 v52, v52
	v_rcp_f32_e32 v53, v53
	v_rcp_f32_e32 v54, v54
	v_rcp_f32_e32 v55, v55
	s_nop 0
	v_pk_mul_f32 v[168:169], v[168:169], v[48:49]
	v_pk_mul_f32 v[170:171], v[170:171], v[50:51]
	v_pk_mul_f32 v[184:185], v[184:185], v[52:53]
	v_pk_mul_f32 v[186:187], v[186:187], v[54:55]
	v_cvt_pk_bf16_f32 v68, v168, v169
	v_cvt_pk_bf16_f32 v69, v170, v171
	v_cvt_pk_bf16_f32 v70, v184, v185
	v_cvt_pk_bf16_f32 v71, v186, v187
	global_store_dwordx2 v18, v[68:69], s[10:11] offset:64
	global_store_dwordx2 v18, v[70:71], s[10:11] offset:96
	v_pk_mul_f32 v[200:201], v[200:201], v[24:25] op_sel_hi:[1,0]
	v_pk_mul_f32 v[202:203], v[202:203], v[24:25] op_sel_hi:[1,0]
	v_pk_mul_f32 v[216:217], v[216:217], v[24:25] op_sel_hi:[1,0]
	v_pk_mul_f32 v[218:219], v[218:219], v[24:25] op_sel_hi:[1,0]
	v_pk_mul_f32 v[32:33], v[200:201], s[26:27]
	v_pk_mul_f32 v[34:35], v[202:203], s[26:27]
	v_pk_mul_f32 v[36:37], v[216:217], s[26:27]
	v_pk_mul_f32 v[38:39], v[218:219], s[26:27]
	v_pk_fma_f32 v[32:33], v[200:201], v[32:33], s[28:29] neg_lo:[1,0,0] neg_hi:[1,0,0]
	v_pk_fma_f32 v[34:35], v[202:203], v[34:35], s[28:29] neg_lo:[1,0,0] neg_hi:[1,0,0]
	v_pk_fma_f32 v[36:37], v[216:217], v[36:37], s[28:29] neg_lo:[1,0,0] neg_hi:[1,0,0]
	v_pk_fma_f32 v[38:39], v[218:219], v[38:39], s[28:29] neg_lo:[1,0,0] neg_hi:[1,0,0]
	v_pk_mul_f32 v[32:33], v[200:201], v[32:33]
	v_pk_mul_f32 v[34:35], v[202:203], v[34:35]
	v_pk_mul_f32 v[36:37], v[216:217], v[36:37]
	v_pk_mul_f32 v[38:39], v[218:219], v[38:39]
	v_exp_f32_e32 v32, v32
	v_exp_f32_e32 v33, v33
	v_exp_f32_e32 v34, v34
	v_exp_f32_e32 v35, v35
	v_exp_f32_e32 v36, v36
	v_exp_f32_e32 v37, v37
	v_exp_f32_e32 v38, v38
	v_exp_f32_e32 v39, v39
	v_pk_add_f32 v[32:33], v[32:33], s[30:31]
	v_pk_add_f32 v[34:35], v[34:35], s[30:31]
	v_pk_add_f32 v[36:37], v[36:37], s[30:31]
	v_pk_add_f32 v[38:39], v[38:39], s[30:31]
	v_rcp_f32_e32 v32, v32
	v_rcp_f32_e32 v33, v33
	v_rcp_f32_e32 v34, v34
	v_rcp_f32_e32 v35, v35
	v_rcp_f32_e32 v36, v36
	v_rcp_f32_e32 v37, v37
	v_rcp_f32_e32 v38, v38
	v_rcp_f32_e32 v39, v39
	s_nop 0
	v_pk_mul_f32 v[200:201], v[200:201], v[32:33]
	v_pk_mul_f32 v[202:203], v[202:203], v[34:35]
	v_pk_mul_f32 v[216:217], v[216:217], v[36:37]
	v_pk_mul_f32 v[218:219], v[218:219], v[38:39]
	v_cvt_pk_bf16_f32 v64, v200, v201
	v_cvt_pk_bf16_f32 v65, v202, v203
	v_cvt_pk_bf16_f32 v66, v216, v217
	v_cvt_pk_bf16_f32 v67, v218, v219
	global_store_dwordx2 v18, v[64:65], s[10:11] offset:128
	global_store_dwordx2 v18, v[66:67], s[10:11] offset:160
	v_pk_mul_f32 v[232:233], v[232:233], v[24:25] op_sel_hi:[1,0]
	v_pk_mul_f32 v[234:235], v[234:235], v[24:25] op_sel_hi:[1,0]
	v_pk_mul_f32 v[248:249], v[248:249], v[24:25] op_sel_hi:[1,0]
	v_pk_mul_f32 v[250:251], v[250:251], v[24:25] op_sel_hi:[1,0]
	v_pk_mul_f32 v[48:49], v[232:233], s[26:27]
	v_pk_mul_f32 v[50:51], v[234:235], s[26:27]
	v_pk_mul_f32 v[52:53], v[248:249], s[26:27]
	v_pk_mul_f32 v[54:55], v[250:251], s[26:27]
	v_pk_fma_f32 v[48:49], v[232:233], v[48:49], s[28:29] neg_lo:[1,0,0] neg_hi:[1,0,0]
	v_pk_fma_f32 v[50:51], v[234:235], v[50:51], s[28:29] neg_lo:[1,0,0] neg_hi:[1,0,0]
	v_pk_fma_f32 v[52:53], v[248:249], v[52:53], s[28:29] neg_lo:[1,0,0] neg_hi:[1,0,0]
	v_pk_fma_f32 v[54:55], v[250:251], v[54:55], s[28:29] neg_lo:[1,0,0] neg_hi:[1,0,0]
	v_pk_mul_f32 v[48:49], v[232:233], v[48:49]
	v_pk_mul_f32 v[50:51], v[234:235], v[50:51]
	v_pk_mul_f32 v[52:53], v[248:249], v[52:53]
	v_pk_mul_f32 v[54:55], v[250:251], v[54:55]
	v_exp_f32_e32 v48, v48
	v_exp_f32_e32 v49, v49
	v_exp_f32_e32 v50, v50
	v_exp_f32_e32 v51, v51
	v_exp_f32_e32 v52, v52
	v_exp_f32_e32 v53, v53
	v_exp_f32_e32 v54, v54
	v_exp_f32_e32 v55, v55
	v_pk_add_f32 v[48:49], v[48:49], s[30:31]
	v_pk_add_f32 v[50:51], v[50:51], s[30:31]
	v_pk_add_f32 v[52:53], v[52:53], s[30:31]
	v_pk_add_f32 v[54:55], v[54:55], s[30:31]
	v_rcp_f32_e32 v48, v48
	v_rcp_f32_e32 v49, v49
	v_rcp_f32_e32 v50, v50
	v_rcp_f32_e32 v51, v51
	v_rcp_f32_e32 v52, v52
	v_rcp_f32_e32 v53, v53
	v_rcp_f32_e32 v54, v54
	v_rcp_f32_e32 v55, v55
	s_nop 0
	v_pk_mul_f32 v[232:233], v[232:233], v[48:49]
	v_pk_mul_f32 v[234:235], v[234:235], v[50:51]
	v_pk_mul_f32 v[248:249], v[248:249], v[52:53]
	v_pk_mul_f32 v[250:251], v[250:251], v[54:55]
	v_cvt_pk_bf16_f32 v68, v232, v233
	v_cvt_pk_bf16_f32 v69, v234, v235
	v_cvt_pk_bf16_f32 v70, v248, v249
	v_cvt_pk_bf16_f32 v71, v250, v251
	global_store_dwordx2 v18, v[68:69], s[10:11] offset:192
	global_store_dwordx2 v18, v[70:71], s[10:11] offset:224
	v_pk_mul_f32 v[140:141], v[140:141], v[26:27] op_sel_hi:[1,0]
	v_pk_mul_f32 v[142:143], v[142:143], v[26:27] op_sel_hi:[1,0]
	v_pk_mul_f32 v[156:157], v[156:157], v[26:27] op_sel_hi:[1,0]
	v_pk_mul_f32 v[158:159], v[158:159], v[26:27] op_sel_hi:[1,0]
	v_pk_mul_f32 v[32:33], v[140:141], s[26:27]
	v_pk_mul_f32 v[34:35], v[142:143], s[26:27]
	v_pk_mul_f32 v[36:37], v[156:157], s[26:27]
	v_pk_mul_f32 v[38:39], v[158:159], s[26:27]
	v_pk_fma_f32 v[32:33], v[140:141], v[32:33], s[28:29] neg_lo:[1,0,0] neg_hi:[1,0,0]
	v_pk_fma_f32 v[34:35], v[142:143], v[34:35], s[28:29] neg_lo:[1,0,0] neg_hi:[1,0,0]
	v_pk_fma_f32 v[36:37], v[156:157], v[36:37], s[28:29] neg_lo:[1,0,0] neg_hi:[1,0,0]
	v_pk_fma_f32 v[38:39], v[158:159], v[38:39], s[28:29] neg_lo:[1,0,0] neg_hi:[1,0,0]
	v_pk_mul_f32 v[32:33], v[140:141], v[32:33]
	v_pk_mul_f32 v[34:35], v[142:143], v[34:35]
	v_pk_mul_f32 v[36:37], v[156:157], v[36:37]
	v_pk_mul_f32 v[38:39], v[158:159], v[38:39]
	v_exp_f32_e32 v32, v32
	v_exp_f32_e32 v33, v33
	v_exp_f32_e32 v34, v34
	v_exp_f32_e32 v35, v35
	v_exp_f32_e32 v36, v36
	v_exp_f32_e32 v37, v37
	v_exp_f32_e32 v38, v38
	v_exp_f32_e32 v39, v39
	v_pk_add_f32 v[32:33], v[32:33], s[30:31]
	v_pk_add_f32 v[34:35], v[34:35], s[30:31]
	v_pk_add_f32 v[36:37], v[36:37], s[30:31]
	v_pk_add_f32 v[38:39], v[38:39], s[30:31]
	v_rcp_f32_e32 v32, v32
	v_rcp_f32_e32 v33, v33
	v_rcp_f32_e32 v34, v34
	v_rcp_f32_e32 v35, v35
	v_rcp_f32_e32 v36, v36
	v_rcp_f32_e32 v37, v37
	v_rcp_f32_e32 v38, v38
	v_rcp_f32_e32 v39, v39
	s_nop 0
	v_pk_mul_f32 v[140:141], v[140:141], v[32:33]
	v_pk_mul_f32 v[142:143], v[142:143], v[34:35]
	v_pk_mul_f32 v[156:157], v[156:157], v[36:37]
	v_pk_mul_f32 v[158:159], v[158:159], v[38:39]
	v_cvt_pk_bf16_f32 v64, v140, v141
	v_cvt_pk_bf16_f32 v65, v142, v143
	v_cvt_pk_bf16_f32 v66, v156, v157
	v_cvt_pk_bf16_f32 v67, v158, v159
	global_store_dwordx2 v19, v[64:65], s[10:11]
	global_store_dwordx2 v19, v[66:67], s[10:11] offset:32
	v_pk_mul_f32 v[172:173], v[172:173], v[26:27] op_sel_hi:[1,0]
	v_pk_mul_f32 v[174:175], v[174:175], v[26:27] op_sel_hi:[1,0]
	v_pk_mul_f32 v[188:189], v[188:189], v[26:27] op_sel_hi:[1,0]
	v_pk_mul_f32 v[190:191], v[190:191], v[26:27] op_sel_hi:[1,0]
	v_pk_mul_f32 v[48:49], v[172:173], s[26:27]
	v_pk_mul_f32 v[50:51], v[174:175], s[26:27]
	v_pk_mul_f32 v[52:53], v[188:189], s[26:27]
	v_pk_mul_f32 v[54:55], v[190:191], s[26:27]
	v_pk_fma_f32 v[48:49], v[172:173], v[48:49], s[28:29] neg_lo:[1,0,0] neg_hi:[1,0,0]
	v_pk_fma_f32 v[50:51], v[174:175], v[50:51], s[28:29] neg_lo:[1,0,0] neg_hi:[1,0,0]
	v_pk_fma_f32 v[52:53], v[188:189], v[52:53], s[28:29] neg_lo:[1,0,0] neg_hi:[1,0,0]
	v_pk_fma_f32 v[54:55], v[190:191], v[54:55], s[28:29] neg_lo:[1,0,0] neg_hi:[1,0,0]
	v_pk_mul_f32 v[48:49], v[172:173], v[48:49]
	v_pk_mul_f32 v[50:51], v[174:175], v[50:51]
	v_pk_mul_f32 v[52:53], v[188:189], v[52:53]
	v_pk_mul_f32 v[54:55], v[190:191], v[54:55]
	v_exp_f32_e32 v48, v48
	v_exp_f32_e32 v49, v49
	v_exp_f32_e32 v50, v50
	v_exp_f32_e32 v51, v51
	v_exp_f32_e32 v52, v52
	v_exp_f32_e32 v53, v53
	v_exp_f32_e32 v54, v54
	v_exp_f32_e32 v55, v55
	v_pk_add_f32 v[48:49], v[48:49], s[30:31]
	v_pk_add_f32 v[50:51], v[50:51], s[30:31]
	v_pk_add_f32 v[52:53], v[52:53], s[30:31]
	v_pk_add_f32 v[54:55], v[54:55], s[30:31]
	v_rcp_f32_e32 v48, v48
	v_rcp_f32_e32 v49, v49
	v_rcp_f32_e32 v50, v50
	v_rcp_f32_e32 v51, v51
	v_rcp_f32_e32 v52, v52
	v_rcp_f32_e32 v53, v53
	v_rcp_f32_e32 v54, v54
	v_rcp_f32_e32 v55, v55
	s_nop 0
	v_pk_mul_f32 v[172:173], v[172:173], v[48:49]
	v_pk_mul_f32 v[174:175], v[174:175], v[50:51]
	v_pk_mul_f32 v[188:189], v[188:189], v[52:53]
	v_pk_mul_f32 v[190:191], v[190:191], v[54:55]
	v_cvt_pk_bf16_f32 v68, v172, v173
	v_cvt_pk_bf16_f32 v69, v174, v175
	v_cvt_pk_bf16_f32 v70, v188, v189
	v_cvt_pk_bf16_f32 v71, v190, v191
	global_store_dwordx2 v19, v[68:69], s[10:11] offset:64
	global_store_dwordx2 v19, v[70:71], s[10:11] offset:96
	v_pk_mul_f32 v[204:205], v[204:205], v[26:27] op_sel_hi:[1,0]
	v_pk_mul_f32 v[206:207], v[206:207], v[26:27] op_sel_hi:[1,0]
	v_pk_mul_f32 v[220:221], v[220:221], v[26:27] op_sel_hi:[1,0]
	v_pk_mul_f32 v[222:223], v[222:223], v[26:27] op_sel_hi:[1,0]
	v_pk_mul_f32 v[32:33], v[204:205], s[26:27]
	v_pk_mul_f32 v[34:35], v[206:207], s[26:27]
	v_pk_mul_f32 v[36:37], v[220:221], s[26:27]
	v_pk_mul_f32 v[38:39], v[222:223], s[26:27]
	v_pk_fma_f32 v[32:33], v[204:205], v[32:33], s[28:29] neg_lo:[1,0,0] neg_hi:[1,0,0]
	v_pk_fma_f32 v[34:35], v[206:207], v[34:35], s[28:29] neg_lo:[1,0,0] neg_hi:[1,0,0]
	v_pk_fma_f32 v[36:37], v[220:221], v[36:37], s[28:29] neg_lo:[1,0,0] neg_hi:[1,0,0]
	v_pk_fma_f32 v[38:39], v[222:223], v[38:39], s[28:29] neg_lo:[1,0,0] neg_hi:[1,0,0]
	v_pk_mul_f32 v[32:33], v[204:205], v[32:33]
	v_pk_mul_f32 v[34:35], v[206:207], v[34:35]
	v_pk_mul_f32 v[36:37], v[220:221], v[36:37]
	v_pk_mul_f32 v[38:39], v[222:223], v[38:39]
	v_exp_f32_e32 v32, v32
	v_exp_f32_e32 v33, v33
	v_exp_f32_e32 v34, v34
	v_exp_f32_e32 v35, v35
	v_exp_f32_e32 v36, v36
	v_exp_f32_e32 v37, v37
	v_exp_f32_e32 v38, v38
	v_exp_f32_e32 v39, v39
	v_pk_add_f32 v[32:33], v[32:33], s[30:31]
	v_pk_add_f32 v[34:35], v[34:35], s[30:31]
	v_pk_add_f32 v[36:37], v[36:37], s[30:31]
	v_pk_add_f32 v[38:39], v[38:39], s[30:31]
	v_rcp_f32_e32 v32, v32
	v_rcp_f32_e32 v33, v33
	v_rcp_f32_e32 v34, v34
	v_rcp_f32_e32 v35, v35
	v_rcp_f32_e32 v36, v36
	v_rcp_f32_e32 v37, v37
	v_rcp_f32_e32 v38, v38
	v_rcp_f32_e32 v39, v39
	s_nop 0
	v_pk_mul_f32 v[204:205], v[204:205], v[32:33]
	v_pk_mul_f32 v[206:207], v[206:207], v[34:35]
	v_pk_mul_f32 v[220:221], v[220:221], v[36:37]
	v_pk_mul_f32 v[222:223], v[222:223], v[38:39]
	v_cvt_pk_bf16_f32 v64, v204, v205
	v_cvt_pk_bf16_f32 v65, v206, v207
	v_cvt_pk_bf16_f32 v66, v220, v221
	v_cvt_pk_bf16_f32 v67, v222, v223
	global_store_dwordx2 v19, v[64:65], s[10:11] offset:128
	global_store_dwordx2 v19, v[66:67], s[10:11] offset:160
	v_pk_mul_f32 v[236:237], v[236:237], v[26:27] op_sel_hi:[1,0]
	v_pk_mul_f32 v[238:239], v[238:239], v[26:27] op_sel_hi:[1,0]
	v_pk_mul_f32 v[252:253], v[252:253], v[26:27] op_sel_hi:[1,0]
	v_pk_mul_f32 v[254:255], v[254:255], v[26:27] op_sel_hi:[1,0]
	v_pk_mul_f32 v[48:49], v[236:237], s[26:27]
	v_pk_mul_f32 v[50:51], v[238:239], s[26:27]
	v_pk_mul_f32 v[52:53], v[252:253], s[26:27]
	v_pk_mul_f32 v[54:55], v[254:255], s[26:27]
	v_pk_fma_f32 v[48:49], v[236:237], v[48:49], s[28:29] neg_lo:[1,0,0] neg_hi:[1,0,0]
	v_pk_fma_f32 v[50:51], v[238:239], v[50:51], s[28:29] neg_lo:[1,0,0] neg_hi:[1,0,0]
	v_pk_fma_f32 v[52:53], v[252:253], v[52:53], s[28:29] neg_lo:[1,0,0] neg_hi:[1,0,0]
	v_pk_fma_f32 v[54:55], v[254:255], v[54:55], s[28:29] neg_lo:[1,0,0] neg_hi:[1,0,0]
	v_pk_mul_f32 v[48:49], v[236:237], v[48:49]
	v_pk_mul_f32 v[50:51], v[238:239], v[50:51]
	v_pk_mul_f32 v[52:53], v[252:253], v[52:53]
	v_pk_mul_f32 v[54:55], v[254:255], v[54:55]
	v_exp_f32_e32 v48, v48
	v_exp_f32_e32 v49, v49
	v_exp_f32_e32 v50, v50
	v_exp_f32_e32 v51, v51
	v_exp_f32_e32 v52, v52
	v_exp_f32_e32 v53, v53
	v_exp_f32_e32 v54, v54
	v_exp_f32_e32 v55, v55
	v_pk_add_f32 v[48:49], v[48:49], s[30:31]
	v_pk_add_f32 v[50:51], v[50:51], s[30:31]
	v_pk_add_f32 v[52:53], v[52:53], s[30:31]
	v_pk_add_f32 v[54:55], v[54:55], s[30:31]
	v_rcp_f32_e32 v48, v48
	v_rcp_f32_e32 v49, v49
	v_rcp_f32_e32 v50, v50
	v_rcp_f32_e32 v51, v51
	v_rcp_f32_e32 v52, v52
	v_rcp_f32_e32 v53, v53
	v_rcp_f32_e32 v54, v54
	v_rcp_f32_e32 v55, v55
	s_nop 0
	v_pk_mul_f32 v[236:237], v[236:237], v[48:49]
	v_pk_mul_f32 v[238:239], v[238:239], v[50:51]
	v_pk_mul_f32 v[252:253], v[252:253], v[52:53]
	v_pk_mul_f32 v[254:255], v[254:255], v[54:55]
	v_cvt_pk_bf16_f32 v68, v236, v237
	v_cvt_pk_bf16_f32 v69, v238, v239
	v_cvt_pk_bf16_f32 v70, v252, v253
	v_cvt_pk_bf16_f32 v71, v254, v255
	global_store_dwordx2 v19, v[68:69], s[10:11] offset:192
	global_store_dwordx2 v19, v[70:71], s[10:11] offset:224

.Ldn_loop:
	s_waitcnt lgkmcnt(0)
	v_mfma_f32_16x16x32_bf16 v[64:67], v[176:179], v[160:163], v[64:67]
	ds_read_b128 v[200:203], v11 offset:0
	v_mfma_f32_16x16x32_bf16 v[68:71], v[176:179], v[164:167], v[68:71]
	ds_read_b128 v[204:207], v11 offset:2048
	v_mfma_f32_16x16x32_bf16 v[72:75], v[176:179], v[168:171], v[72:75]
	ds_read_b128 v[208:211], v11 offset:4096
	v_mfma_f32_16x16x32_bf16 v[76:79], v[176:179], v[172:175], v[76:79]
	ds_read_b128 v[212:215], v11 offset:6144
	v_mfma_f32_16x16x32_bf16 v[80:83], v[180:183], v[160:163], v[80:83]
	ds_read_b128 v[216:219], v13 offset:0
	v_mfma_f32_16x16x32_bf16 v[84:87], v[180:183], v[164:167], v[84:87]
	ds_read_b128 v[220:223], v13 offset:2048
	v_mfma_f32_16x16x32_bf16 v[88:91], v[180:183], v[168:171], v[88:91]
	ds_read_b128 v[224:227], v13 offset:4096
	v_mfma_f32_16x16x32_bf16 v[92:95], v[180:183], v[172:175], v[92:95]
	ds_read_b128 v[228:231], v13 offset:6144
	v_mfma_f32_16x16x32_bf16 v[96:99], v[184:187], v[160:163], v[96:99]
	ds_read_b128 v[232:235], v13 offset:8192
	v_mfma_f32_16x16x32_bf16 v[100:103], v[184:187], v[164:167], v[100:103]
	ds_read_b128 v[236:239], v13 offset:10240
	v_mfma_f32_16x16x32_bf16 v[104:107], v[184:187], v[168:171], v[104:107]
	s_add_u32 m0, s20, 0x5000
	v_mfma_f32_16x16x32_bf16 v[108:111], v[184:187], v[172:175], v[108:111]
	global_load_lds_dwordx4 v3, s[18:19]
	v_mfma_f32_16x16x32_bf16 v[112:115], v[188:191], v[160:163], v[112:115]
	s_add_u32 m0, s20, 0x6000
	v_mfma_f32_16x16x32_bf16 v[116:119], v[188:191], v[164:167], v[116:119]
	global_load_lds_dwordx4 v4, s[18:19]
	v_mfma_f32_16x16x32_bf16 v[120:123], v[188:191], v[168:171], v[120:123]
	s_add_u32 m0, s20, 0x7000
	v_mfma_f32_16x16x32_bf16 v[124:127], v[188:191], v[172:175], v[124:127]
	global_load_lds_dwordx4 v5, s[18:19]
	v_mfma_f32_16x16x32_bf16 v[128:131], v[192:195], v[160:163], v[128:131]
	s_add_u32 m0, s20, 0x8000
	v_mfma_f32_16x16x32_bf16 v[132:135], v[192:195], v[164:167], v[132:135]
	global_load_lds_dwordx4 v6, s[18:19]
	v_mfma_f32_16x16x32_bf16 v[136:139], v[192:195], v[168:171], v[136:139]
	s_add_u32 m0, s20, 0x9000
	v_mfma_f32_16x16x32_bf16 v[140:143], v[192:195], v[172:175], v[140:143]
	global_load_lds_dwordx4 v7, s[18:19]
	v_mfma_f32_16x16x32_bf16 v[144:147], v[196:199], v[160:163], v[144:147]
	s_add_u32 s16, s16, 0x80
	s_addc_u32 s17, s17, 0
	s_add_u32 s18, s18, 0x80
	s_addc_u32 s19, s19, 0
	v_mfma_f32_16x16x32_bf16 v[148:151], v[196:199], v[164:167], v[148:151]
	s_add_u32 s20, s20, 0xa000
	s_sub_u32 s22, s20, 0x28000
	s_cmp_ge_u32 s20, 0x28000
	s_cselect_b32 s20, s22, s20
	v_mfma_f32_16x16x32_bf16 v[152:155], v[196:199], v[168:171], v[152:155]
	v_add_u32_e32 v10, s21, v8
	v_add_u32_e32 v12, s21, v9
	v_xor_b32_e32 v11, 64, v10
	v_xor_b32_e32 v13, 64, v12
	v_mfma_f32_16x16x32_bf16 v[156:159], v[196:199], v[172:175], v[156:159]
	s_add_u32 s21, s21, 0xa000
	s_sub_u32 s23, s21, 0x28000
	s_cmp_ge_u32 s21, 0x28000
	s_cselect_b32 s21, s23, s21
	s_waitcnt lgkmcnt(0)
	v_mfma_f32_16x16x32_bf16 v[64:67], v[216:219], v[200:203], v[64:67]
	v_mfma_f32_16x16x32_bf16 v[68:71], v[216:219], v[204:207], v[68:71]
	v_mfma_f32_16x16x32_bf16 v[72:75], v[216:219], v[208:211], v[72:75]
	v_mfma_f32_16x16x32_bf16 v[76:79], v[216:219], v[212:215], v[76:79]
	s_waitcnt vmcnt(20)
	s_barrier
	v_mfma_f32_16x16x32_bf16 v[80:83], v[220:223], v[200:203], v[80:83]
	ds_read_b128 v[160:163], v10 offset:0
	v_mfma_f32_16x16x32_bf16 v[84:87], v[220:223], v[204:207], v[84:87]
	ds_read_b128 v[164:167], v10 offset:2048
	v_mfma_f32_16x16x32_bf16 v[88:91], v[220:223], v[208:211], v[88:91]
	ds_read_b128 v[168:171], v10 offset:4096
	v_mfma_f32_16x16x32_bf16 v[92:95], v[220:223], v[212:215], v[92:95]
	ds_read_b128 v[172:175], v10 offset:6144
	v_mfma_f32_16x16x32_bf16 v[96:99], v[224:227], v[200:203], v[96:99]
	ds_read_b128 v[176:179], v12 offset:0
	v_mfma_f32_16x16x32_bf16 v[100:103], v[224:227], v[204:207], v[100:103]
	ds_read_b128 v[180:183], v12 offset:2048
	v_mfma_f32_16x16x32_bf16 v[104:107], v[224:227], v[208:211], v[104:107]
	ds_read_b128 v[184:187], v12 offset:4096
	v_mfma_f32_16x16x32_bf16 v[108:111], v[224:227], v[212:215], v[108:111]
	ds_read_b128 v[188:191], v12 offset:6144
	v_mfma_f32_16x16x32_bf16 v[112:115], v[228:231], v[200:203], v[112:115]
	ds_read_b128 v[192:195], v12 offset:8192
	v_mfma_f32_16x16x32_bf16 v[116:119], v[228:231], v[204:207], v[116:119]
	ds_read_b128 v[196:199], v12 offset:10240
	v_mfma_f32_16x16x32_bf16 v[120:123], v[228:231], v[208:211], v[120:123]
	s_add_u32 m0, s20, 0x0
	v_mfma_f32_16x16x32_bf16 v[124:127], v[228:231], v[212:215], v[124:127]
	global_load_lds_dwordx4 v2, s[16:17]
	v_mfma_f32_16x16x32_bf16 v[128:131], v[232:235], v[200:203], v[128:131]
	s_add_u32 m0, s20, 0x1000
	v_mfma_f32_16x16x32_bf16 v[132:135], v[232:235], v[204:207], v[132:135]
	global_load_lds_dwordx4 v3, s[16:17]
	v_mfma_f32_16x16x32_bf16 v[136:139], v[232:235], v[208:211], v[136:139]
	s_add_u32 m0, s20, 0x2000
	v_mfma_f32_16x16x32_bf16 v[140:143], v[232:235], v[212:215], v[140:143]
	global_load_lds_dwordx4 v4, s[16:17]
	v_mfma_f32_16x16x32_bf16 v[144:147], v[236:239], v[200:203], v[144:147]
	s_add_u32 m0, s20, 0x3000
	v_mfma_f32_16x16x32_bf16 v[148:151], v[236:239], v[204:207], v[148:151]
	global_load_lds_dwordx4 v5, s[16:17]
	v_mfma_f32_16x16x32_bf16 v[152:155], v[236:239], v[208:211], v[152:155]
	s_add_u32 m0, s20, 0x4000
	v_mfma_f32_16x16x32_bf16 v[156:159], v[236:239], v[212:215], v[156:159]
	global_load_lds_dwordx4 v2, s[18:19]
	s_add_u32 s15, s15, 1
	s_cmp_lt_u32 s15, 44
	s_cbranch_scc1 .Ldn_loop
	s_waitcnt lgkmcnt(0)
	v_mfma_f32_16x16x32_bf16 v[64:67], v[176:179], v[160:163], v[64:67]
	ds_read_b128 v[200:203], v11 offset:0
	v_mfma_f32_16x16x32_bf16 v[68:71], v[176:179], v[164:167], v[68:71]
	ds_read_b128 v[204:207], v11 offset:2048
	v_mfma_f32_16x16x32_bf16 v[72:75], v[176:179], v[168:171], v[72:75]
	ds_read_b128 v[208:211], v11 offset:4096
	v_mfma_f32_16x16x32_bf16 v[76:79], v[176:179], v[172:175], v[76:79]
	ds_read_b128 v[212:215], v11 offset:6144
	v_mfma_f32_16x16x32_bf16 v[80:83], v[180:183], v[160:163], v[80:83]
	ds_read_b128 v[216:219], v13 offset:0
	v_mfma_f32_16x16x32_bf16 v[84:87], v[180:183], v[164:167], v[84:87]
	ds_read_b128 v[220:223], v13 offset:2048
	v_mfma_f32_16x16x32_bf16 v[88:91], v[180:183], v[168:171], v[88:91]
	ds_read_b128 v[224:227], v13 offset:4096
	v_mfma_f32_16x16x32_bf16 v[92:95], v[180:183], v[172:175], v[92:95]
	ds_read_b128 v[228:231], v13 offset:6144
	v_mfma_f32_16x16x32_bf16 v[96:99], v[184:187], v[160:163], v[96:99]
	ds_read_b128 v[232:235], v13 offset:8192
	v_mfma_f32_16x16x32_bf16 v[100:103], v[184:187], v[164:167], v[100:103]
	ds_read_b128 v[236:239], v13 offset:10240
	v_mfma_f32_16x16x32_bf16 v[104:107], v[184:187], v[168:171], v[104:107]
	s_add_u32 m0, s20, 0x5000
	v_mfma_f32_16x16x32_bf16 v[108:111], v[184:187], v[172:175], v[108:111]
	global_load_lds_dwordx4 v3, s[18:19]
	v_mfma_f32_16x16x32_bf16 v[112:115], v[188:191], v[160:163], v[112:115]
	s_add_u32 m0, s20, 0x6000
	v_mfma_f32_16x16x32_bf16 v[116:119], v[188:191], v[164:167], v[116:119]
	global_load_lds_dwordx4 v4, s[18:19]
	v_mfma_f32_16x16x32_bf16 v[120:123], v[188:191], v[168:171], v[120:123]
	s_add_u32 m0, s20, 0x7000
	v_mfma_f32_16x16x32_bf16 v[124:127], v[188:191], v[172:175], v[124:127]
	global_load_lds_dwordx4 v5, s[18:19]
	v_mfma_f32_16x16x32_bf16 v[128:131], v[192:195], v[160:163], v[128:131]
	s_add_u32 m0, s20, 0x8000
	v_mfma_f32_16x16x32_bf16 v[132:135], v[192:195], v[164:167], v[132:135]
	global_load_lds_dwordx4 v6, s[18:19]
	v_mfma_f32_16x16x32_bf16 v[136:139], v[192:195], v[168:171], v[136:139]
	s_add_u32 m0, s20, 0x9000
	v_mfma_f32_16x16x32_bf16 v[140:143], v[192:195], v[172:175], v[140:143]
	global_load_lds_dwordx4 v7, s[18:19]
	v_mfma_f32_16x16x32_bf16 v[144:147], v[196:199], v[160:163], v[144:147]
	s_add_u32 s16, s16, 0x80
	s_addc_u32 s17, s17, 0
	s_add_u32 s18, s18, 0x80
	s_addc_u32 s19, s19, 0
	v_mfma_f32_16x16x32_bf16 v[148:151], v[196:199], v[164:167], v[148:151]
	s_add_u32 s20, s20, 0xa000
	s_sub_u32 s22, s20, 0x28000
	s_cmp_ge_u32 s20, 0x28000
	s_cselect_b32 s20, s22, s20
	v_mfma_f32_16x16x32_bf16 v[152:155], v[196:199], v[168:171], v[152:155]
	v_add_u32_e32 v10, s21, v8
	v_add_u32_e32 v12, s21, v9
	v_xor_b32_e32 v11, 64, v10
	v_xor_b32_e32 v13, 64, v12
	v_mfma_f32_16x16x32_bf16 v[156:159], v[196:199], v[172:175], v[156:159]
	s_add_u32 s21, s21, 0xa000
	s_sub_u32 s23, s21, 0x28000
	s_cmp_ge_u32 s21, 0x28000
	s_cselect_b32 s21, s23, s21
	s_waitcnt lgkmcnt(0)
	v_mfma_f32_16x16x32_bf16 v[64:67], v[216:219], v[200:203], v[64:67]
	v_mfma_f32_16x16x32_bf16 v[68:71], v[216:219], v[204:207], v[68:71]
	v_mfma_f32_16x16x32_bf16 v[72:75], v[216:219], v[208:211], v[72:75]
	v_mfma_f32_16x16x32_bf16 v[76:79], v[216:219], v[212:215], v[76:79]
	s_waitcnt vmcnt(20)
	s_barrier
	v_mfma_f32_16x16x32_bf16 v[80:83], v[220:223], v[200:203], v[80:83]
	ds_read_b128 v[160:163], v10 offset:0
	v_mfma_f32_16x16x32_bf16 v[84:87], v[220:223], v[204:207], v[84:87]
	ds_read_b128 v[164:167], v10 offset:2048
	v_mfma_f32_16x16x32_bf16 v[88:91], v[220:223], v[208:211], v[88:91]
	ds_read_b128 v[168:171], v10 offset:4096
	v_mfma_f32_16x16x32_bf16 v[92:95], v[220:223], v[212:215], v[92:95]
	ds_read_b128 v[172:175], v10 offset:6144
	v_mfma_f32_16x16x32_bf16 v[96:99], v[224:227], v[200:203], v[96:99]
	ds_read_b128 v[176:179], v12 offset:0
	v_mfma_f32_16x16x32_bf16 v[100:103], v[224:227], v[204:207], v[100:103]
	ds_read_b128 v[180:183], v12 offset:2048
	v_mfma_f32_16x16x32_bf16 v[104:107], v[224:227], v[208:211], v[104:107]
	ds_read_b128 v[184:187], v12 offset:4096
	v_mfma_f32_16x16x32_bf16 v[108:111], v[224:227], v[212:215], v[108:111]
	ds_read_b128 v[188:191], v12 offset:6144
	v_mfma_f32_16x16x32_bf16 v[112:115], v[228:231], v[200:203], v[112:115]
	ds_read_b128 v[192:195], v12 offset:8192
	v_mfma_f32_16x16x32_bf16 v[116:119], v[228:231], v[204:207], v[116:119]
	ds_read_b128 v[196:199], v12 offset:10240
	v_mfma_f32_16x16x32_bf16 v[120:123], v[228:231], v[208:211], v[120:123]
	global_load_dwordx4 v[16:19], v56, s[8:9] offset:0
	v_mfma_f32_16x16x32_bf16 v[124:127], v[228:231], v[212:215], v[124:127]
	global_load_dwordx4 v[20:23], v57, s[8:9] offset:0
	v_mfma_f32_16x16x32_bf16 v[128:131], v[232:235], v[200:203], v[128:131]
	global_load_dwordx4 v[24:27], v58, s[8:9] offset:0
	v_mfma_f32_16x16x32_bf16 v[132:135], v[232:235], v[204:207], v[132:135]
	global_load_dwordx4 v[28:31], v59, s[8:9] offset:0
	v_mfma_f32_16x16x32_bf16 v[136:139], v[232:235], v[208:211], v[136:139]
	global_load_dwordx4 v[32:35], v56, s[8:9] offset:64
	v_mfma_f32_16x16x32_bf16 v[140:143], v[232:235], v[212:215], v[140:143]
	global_load_dwordx4 v[36:39], v57, s[8:9] offset:64
	v_mfma_f32_16x16x32_bf16 v[144:147], v[236:239], v[200:203], v[144:147]
	global_load_dwordx4 v[40:43], v58, s[8:9] offset:64
	v_mfma_f32_16x16x32_bf16 v[148:151], v[236:239], v[204:207], v[148:151]
	global_load_dwordx4 v[44:47], v59, s[8:9] offset:64
	v_mfma_f32_16x16x32_bf16 v[152:155], v[236:239], v[208:211], v[152:155]
	global_load_dwordx4 v[48:51], v56, s[8:9] offset:128
	v_mfma_f32_16x16x32_bf16 v[156:159], v[236:239], v[212:215], v[156:159]
	global_load_dwordx4 v[52:55], v57, s[8:9] offset:128
	global_load_dwordx4 v[240:243], v58, s[8:9] offset:128
	global_load_dwordx4 v[244:247], v59, s[8:9] offset:128
	global_load_dwordx4 v[248:251], v56, s[8:9] offset:192
	global_load_dwordx4 v[252:255], v57, s[8:9] offset:192
	s_waitcnt lgkmcnt(0)
	v_mfma_f32_16x16x32_bf16 v[64:67], v[176:179], v[160:163], v[64:67]
	ds_read_b128 v[200:203], v11 offset:0
	v_mfma_f32_16x16x32_bf16 v[68:71], v[176:179], v[164:167], v[68:71]
	ds_read_b128 v[204:207], v11 offset:2048
	v_mfma_f32_16x16x32_bf16 v[72:75], v[176:179], v[168:171], v[72:75]
	ds_read_b128 v[208:211], v11 offset:4096
	v_mfma_f32_16x16x32_bf16 v[76:79], v[176:179], v[172:175], v[76:79]
	ds_read_b128 v[212:215], v11 offset:6144
	v_mfma_f32_16x16x32_bf16 v[80:83], v[180:183], v[160:163], v[80:83]
	ds_read_b128 v[216:219], v13 offset:0
	v_mfma_f32_16x16x32_bf16 v[84:87], v[180:183], v[164:167], v[84:87]
	ds_read_b128 v[220:223], v13 offset:2048
	v_mfma_f32_16x16x32_bf16 v[88:91], v[180:183], v[168:171], v[88:91]
	ds_read_b128 v[224:227], v13 offset:4096
	v_mfma_f32_16x16x32_bf16 v[92:95], v[180:183], v[172:175], v[92:95]
	ds_read_b128 v[228:231], v13 offset:6144
	v_mfma_f32_16x16x32_bf16 v[96:99], v[184:187], v[160:163], v[96:99]
	ds_read_b128 v[232:235], v13 offset:8192
	v_mfma_f32_16x16x32_bf16 v[100:103], v[184:187], v[164:167], v[100:103]
	ds_read_b128 v[236:239], v13 offset:10240
	v_mfma_f32_16x16x32_bf16 v[104:107], v[184:187], v[168:171], v[104:107]
	v_mfma_f32_16x16x32_bf16 v[108:111], v[184:187], v[172:175], v[108:111]
	v_mfma_f32_16x16x32_bf16 v[112:115], v[188:191], v[160:163], v[112:115]
	v_mfma_f32_16x16x32_bf16 v[116:119], v[188:191], v[164:167], v[116:119]
	v_mfma_f32_16x16x32_bf16 v[120:123], v[188:191], v[168:171], v[120:123]
	v_mfma_f32_16x16x32_bf16 v[124:127], v[188:191], v[172:175], v[124:127]
	v_mfma_f32_16x16x32_bf16 v[128:131], v[192:195], v[160:163], v[128:131]
	v_mfma_f32_16x16x32_bf16 v[132:135], v[192:195], v[164:167], v[132:135]
	v_mfma_f32_16x16x32_bf16 v[136:139], v[192:195], v[168:171], v[136:139]
	v_mfma_f32_16x16x32_bf16 v[140:143], v[192:195], v[172:175], v[140:143]
	v_mfma_f32_16x16x32_bf16 v[144:147], v[196:199], v[160:163], v[144:147]
	v_add_u32_e32 v10, s21, v8
	v_add_u32_e32 v12, s21, v9
	v_xor_b32_e32 v11, 64, v10
	v_xor_b32_e32 v13, 64, v12
	v_mfma_f32_16x16x32_bf16 v[148:151], v[196:199], v[164:167], v[148:151]
	s_add_u32 s21, s21, 0xa000
	s_sub_u32 s23, s21, 0x28000
	s_cmp_ge_u32 s21, 0x28000
	s_cselect_b32 s21, s23, s21
	v_mfma_f32_16x16x32_bf16 v[152:155], v[196:199], v[168:171], v[152:155]
	v_mfma_f32_16x16x32_bf16 v[156:159], v[196:199], v[172:175], v[156:159]
	s_waitcnt lgkmcnt(0)
	v_mfma_f32_16x16x32_bf16 v[64:67], v[216:219], v[200:203], v[64:67]
	v_mfma_f32_16x16x32_bf16 v[68:71], v[216:219], v[204:207], v[68:71]
	v_mfma_f32_16x16x32_bf16 v[72:75], v[216:219], v[208:211], v[72:75]
	v_mfma_f32_16x16x32_bf16 v[76:79], v[216:219], v[212:215], v[76:79]
	s_waitcnt vmcnt(24)
	s_barrier
	v_mfma_f32_16x16x32_bf16 v[80:83], v[220:223], v[200:203], v[80:83]
	ds_read_b128 v[160:163], v10 offset:0
	v_mfma_f32_16x16x32_bf16 v[84:87], v[220:223], v[204:207], v[84:87]
	ds_read_b128 v[164:167], v10 offset:2048
	v_mfma_f32_16x16x32_bf16 v[88:91], v[220:223], v[208:211], v[88:91]
	ds_read_b128 v[168:171], v10 offset:4096
	v_mfma_f32_16x16x32_bf16 v[92:95], v[220:223], v[212:215], v[92:95]
	ds_read_b128 v[172:175], v10 offset:6144
	v_mfma_f32_16x16x32_bf16 v[96:99], v[224:227], v[200:203], v[96:99]
	ds_read_b128 v[176:179], v12 offset:0
	v_mfma_f32_16x16x32_bf16 v[100:103], v[224:227], v[204:207], v[100:103]
	ds_read_b128 v[180:183], v12 offset:2048
	v_mfma_f32_16x16x32_bf16 v[104:107], v[224:227], v[208:211], v[104:107]
	ds_read_b128 v[184:187], v12 offset:4096
	v_mfma_f32_16x16x32_bf16 v[108:111], v[224:227], v[212:215], v[108:111]
	ds_read_b128 v[188:191], v12 offset:6144
	v_mfma_f32_16x16x32_bf16 v[112:115], v[228:231], v[200:203], v[112:115]
	ds_read_b128 v[192:195], v12 offset:8192
	v_mfma_f32_16x16x32_bf16 v[116:119], v[228:231], v[204:207], v[116:119]
	ds_read_b128 v[196:199], v12 offset:10240
	v_mfma_f32_16x16x32_bf16 v[120:123], v[228:231], v[208:211], v[120:123]
	v_mfma_f32_16x16x32_bf16 v[124:127], v[228:231], v[212:215], v[124:127]
	v_mfma_f32_16x16x32_bf16 v[128:131], v[232:235], v[200:203], v[128:131]
	v_mfma_f32_16x16x32_bf16 v[132:135], v[232:235], v[204:207], v[132:135]
	v_mfma_f32_16x16x32_bf16 v[136:139], v[232:235], v[208:211], v[136:139]
	v_mfma_f32_16x16x32_bf16 v[140:143], v[232:235], v[212:215], v[140:143]
	v_mfma_f32_16x16x32_bf16 v[144:147], v[236:239], v[200:203], v[144:147]
	v_mfma_f32_16x16x32_bf16 v[148:151], v[236:239], v[204:207], v[148:151]
	v_mfma_f32_16x16x32_bf16 v[152:155], v[236:239], v[208:211], v[152:155]
	v_mfma_f32_16x16x32_bf16 v[156:159], v[236:239], v[212:215], v[156:159]
	s_waitcnt lgkmcnt(0)
	v_mfma_f32_16x16x32_bf16 v[64:67], v[176:179], v[160:163], v[64:67]
	ds_read_b128 v[200:203], v11 offset:0
	v_mfma_f32_16x16x32_bf16 v[68:71], v[176:179], v[164:167], v[68:71]
	ds_read_b128 v[204:207], v11 offset:2048
	v_mfma_f32_16x16x32_bf16 v[72:75], v[176:179], v[168:171], v[72:75]
	ds_read_b128 v[208:211], v11 offset:4096
	v_mfma_f32_16x16x32_bf16 v[76:79], v[176:179], v[172:175], v[76:79]
	ds_read_b128 v[212:215], v11 offset:6144
	v_mfma_f32_16x16x32_bf16 v[80:83], v[180:183], v[160:163], v[80:83]
	ds_read_b128 v[216:219], v13 offset:0
	v_mfma_f32_16x16x32_bf16 v[84:87], v[180:183], v[164:167], v[84:87]
	ds_read_b128 v[220:223], v13 offset:2048
	v_mfma_f32_16x16x32_bf16 v[88:91], v[180:183], v[168:171], v[88:91]
	ds_read_b128 v[224:227], v13 offset:4096
	v_mfma_f32_16x16x32_bf16 v[92:95], v[180:183], v[172:175], v[92:95]
	ds_read_b128 v[228:231], v13 offset:6144
	v_mfma_f32_16x16x32_bf16 v[96:99], v[184:187], v[160:163], v[96:99]
	ds_read_b128 v[232:235], v13 offset:8192
	v_mfma_f32_16x16x32_bf16 v[100:103], v[184:187], v[164:167], v[100:103]
	ds_read_b128 v[236:239], v13 offset:10240
	v_mfma_f32_16x16x32_bf16 v[104:107], v[184:187], v[168:171], v[104:107]
	v_mfma_f32_16x16x32_bf16 v[108:111], v[184:187], v[172:175], v[108:111]
	v_mfma_f32_16x16x32_bf16 v[112:115], v[188:191], v[160:163], v[112:115]
	v_mfma_f32_16x16x32_bf16 v[116:119], v[188:191], v[164:167], v[116:119]
	v_mfma_f32_16x16x32_bf16 v[120:123], v[188:191], v[168:171], v[120:123]
	v_mfma_f32_16x16x32_bf16 v[124:127], v[188:191], v[172:175], v[124:127]
	v_mfma_f32_16x16x32_bf16 v[128:131], v[192:195], v[160:163], v[128:131]
	v_mfma_f32_16x16x32_bf16 v[132:135], v[192:195], v[164:167], v[132:135]
	v_mfma_f32_16x16x32_bf16 v[136:139], v[192:195], v[168:171], v[136:139]
	v_mfma_f32_16x16x32_bf16 v[140:143], v[192:195], v[172:175], v[140:143]
	v_mfma_f32_16x16x32_bf16 v[144:147], v[196:199], v[160:163], v[144:147]
	v_add_u32_e32 v10, s21, v8
	v_add_u32_e32 v12, s21, v9
	v_xor_b32_e32 v11, 64, v10
	v_xor_b32_e32 v13, 64, v12
	v_mfma_f32_16x16x32_bf16 v[148:151], v[196:199], v[164:167], v[148:151]
	s_add_u32 s21, s21, 0xa000
	s_sub_u32 s23, s21, 0x28000
	s_cmp_ge_u32 s21, 0x28000
	s_cselect_b32 s21, s23, s21
	v_mfma_f32_16x16x32_bf16 v[152:155], v[196:199], v[168:171], v[152:155]
	v_mfma_f32_16x16x32_bf16 v[156:159], v[196:199], v[172:175], v[156:159]
	s_waitcnt lgkmcnt(0)
	v_mfma_f32_16x16x32_bf16 v[64:67], v[216:219], v[200:203], v[64:67]
	v_mfma_f32_16x16x32_bf16 v[68:71], v[216:219], v[204:207], v[68:71]
	v_mfma_f32_16x16x32_bf16 v[72:75], v[216:219], v[208:211], v[72:75]
	v_mfma_f32_16x16x32_bf16 v[76:79], v[216:219], v[212:215], v[76:79]
	s_waitcnt vmcnt(14)
	s_barrier
	v_mfma_f32_16x16x32_bf16 v[80:83], v[220:223], v[200:203], v[80:83]
	ds_read_b128 v[160:163], v10 offset:0
	v_mfma_f32_16x16x32_bf16 v[84:87], v[220:223], v[204:207], v[84:87]
	ds_read_b128 v[164:167], v10 offset:2048
	v_mfma_f32_16x16x32_bf16 v[88:91], v[220:223], v[208:211], v[88:91]
	ds_read_b128 v[168:171], v10 offset:4096
	v_mfma_f32_16x16x32_bf16 v[92:95], v[220:223], v[212:215], v[92:95]
	ds_read_b128 v[172:175], v10 offset:6144
	v_mfma_f32_16x16x32_bf16 v[96:99], v[224:227], v[200:203], v[96:99]
	ds_read_b128 v[176:179], v12 offset:0
	v_mfma_f32_16x16x32_bf16 v[100:103], v[224:227], v[204:207], v[100:103]
	ds_read_b128 v[180:183], v12 offset:2048
	v_mfma_f32_16x16x32_bf16 v[104:107], v[224:227], v[208:211], v[104:107]
	ds_read_b128 v[184:187], v12 offset:4096
	v_mfma_f32_16x16x32_bf16 v[108:111], v[224:227], v[212:215], v[108:111]
	ds_read_b128 v[188:191], v12 offset:6144
	v_mfma_f32_16x16x32_bf16 v[112:115], v[228:231], v[200:203], v[112:115]
	ds_read_b128 v[192:195], v12 offset:8192
	v_mfma_f32_16x16x32_bf16 v[116:119], v[228:231], v[204:207], v[116:119]
	ds_read_b128 v[196:199], v12 offset:10240
	v_mfma_f32_16x16x32_bf16 v[120:123], v[228:231], v[208:211], v[120:123]
	v_mfma_f32_16x16x32_bf16 v[124:127], v[228:231], v[212:215], v[124:127]
	v_mfma_f32_16x16x32_bf16 v[128:131], v[232:235], v[200:203], v[128:131]
	v_mfma_f32_16x16x32_bf16 v[132:135], v[232:235], v[204:207], v[132:135]
	v_mfma_f32_16x16x32_bf16 v[136:139], v[232:235], v[208:211], v[136:139]
	v_mfma_f32_16x16x32_bf16 v[140:143], v[232:235], v[212:215], v[140:143]
	v_mfma_f32_16x16x32_bf16 v[144:147], v[236:239], v[200:203], v[144:147]
	v_mfma_f32_16x16x32_bf16 v[148:151], v[236:239], v[204:207], v[148:151]
	v_mfma_f32_16x16x32_bf16 v[152:155], v[236:239], v[208:211], v[152:155]
	v_mfma_f32_16x16x32_bf16 v[156:159], v[236:239], v[212:215], v[156:159]
	s_waitcnt lgkmcnt(0)
	v_mfma_f32_16x16x32_bf16 v[64:67], v[176:179], v[160:163], v[64:67]
	ds_read_b128 v[200:203], v11 offset:0
	v_mfma_f32_16x16x32_bf16 v[68:71], v[176:179], v[164:167], v[68:71]
	ds_read_b128 v[204:207], v11 offset:2048
	v_mfma_f32_16x16x32_bf16 v[72:75], v[176:179], v[168:171], v[72:75]
	ds_read_b128 v[208:211], v11 offset:4096
	v_mfma_f32_16x16x32_bf16 v[76:79], v[176:179], v[172:175], v[76:79]
	ds_read_b128 v[212:215], v11 offset:6144
	v_mfma_f32_16x16x32_bf16 v[80:83], v[180:183], v[160:163], v[80:83]
	ds_read_b128 v[216:219], v13 offset:0
	v_mfma_f32_16x16x32_bf16 v[84:87], v[180:183], v[164:167], v[84:87]
	ds_read_b128 v[220:223], v13 offset:2048
	v_mfma_f32_16x16x32_bf16 v[88:91], v[180:183], v[168:171], v[88:91]
	ds_read_b128 v[224:227], v13 offset:4096
	v_mfma_f32_16x16x32_bf16 v[92:95], v[180:183], v[172:175], v[92:95]
	ds_read_b128 v[228:231], v13 offset:6144
	v_mfma_f32_16x16x32_bf16 v[96:99], v[184:187], v[160:163], v[96:99]
	ds_read_b128 v[232:235], v13 offset:8192
	v_mfma_f32_16x16x32_bf16 v[100:103], v[184:187], v[164:167], v[100:103]
	ds_read_b128 v[236:239], v13 offset:10240
	v_mfma_f32_16x16x32_bf16 v[104:107], v[184:187], v[168:171], v[104:107]
	v_mfma_f32_16x16x32_bf16 v[108:111], v[184:187], v[172:175], v[108:111]
	v_mfma_f32_16x16x32_bf16 v[112:115], v[188:191], v[160:163], v[112:115]
	v_mfma_f32_16x16x32_bf16 v[116:119], v[188:191], v[164:167], v[116:119]
	v_mfma_f32_16x16x32_bf16 v[120:123], v[188:191], v[168:171], v[120:123]
	v_mfma_f32_16x16x32_bf16 v[124:127], v[188:191], v[172:175], v[124:127]
	v_mfma_f32_16x16x32_bf16 v[128:131], v[192:195], v[160:163], v[128:131]
	v_mfma_f32_16x16x32_bf16 v[132:135], v[192:195], v[164:167], v[132:135]
	v_mfma_f32_16x16x32_bf16 v[136:139], v[192:195], v[168:171], v[136:139]
	v_mfma_f32_16x16x32_bf16 v[140:143], v[192:195], v[172:175], v[140:143]
	v_mfma_f32_16x16x32_bf16 v[144:147], v[196:199], v[160:163], v[144:147]
	v_mfma_f32_16x16x32_bf16 v[148:151], v[196:199], v[164:167], v[148:151]
	v_mfma_f32_16x16x32_bf16 v[152:155], v[196:199], v[168:171], v[152:155]
	v_mfma_f32_16x16x32_bf16 v[156:159], v[196:199], v[172:175], v[156:159]
	s_waitcnt lgkmcnt(0)
	v_mfma_f32_16x16x32_bf16 v[64:67], v[216:219], v[200:203], v[64:67]
	v_mfma_f32_16x16x32_bf16 v[68:71], v[216:219], v[204:207], v[68:71]
	global_load_dwordx4 v[160:163], v58, s[8:9] offset:192
	v_mfma_f32_16x16x32_bf16 v[72:75], v[216:219], v[208:211], v[72:75]
	v_mfma_f32_16x16x32_bf16 v[76:79], v[216:219], v[212:215], v[76:79]
	global_load_dwordx4 v[164:167], v59, s[8:9] offset:192
	v_mfma_f32_16x16x32_bf16 v[80:83], v[220:223], v[200:203], v[80:83]
	v_mfma_f32_16x16x32_bf16 v[84:87], v[220:223], v[204:207], v[84:87]
	global_load_dwordx4 v[168:171], v56, s[8:9] offset:256
	v_mfma_f32_16x16x32_bf16 v[88:91], v[220:223], v[208:211], v[88:91]
	v_mfma_f32_16x16x32_bf16 v[92:95], v[220:223], v[212:215], v[92:95]
	global_load_dwordx4 v[172:175], v57, s[8:9] offset:256
	v_mfma_f32_16x16x32_bf16 v[96:99], v[224:227], v[200:203], v[96:99]
	v_mfma_f32_16x16x32_bf16 v[100:103], v[224:227], v[204:207], v[100:103]
	global_load_dwordx4 v[176:179], v58, s[8:9] offset:256
	v_mfma_f32_16x16x32_bf16 v[104:107], v[224:227], v[208:211], v[104:107]
	v_mfma_f32_16x16x32_bf16 v[108:111], v[224:227], v[212:215], v[108:111]
	global_load_dwordx4 v[180:183], v59, s[8:9] offset:256
	v_mfma_f32_16x16x32_bf16 v[112:115], v[228:231], v[200:203], v[112:115]
	v_mfma_f32_16x16x32_bf16 v[116:119], v[228:231], v[204:207], v[116:119]
	global_load_dwordx4 v[184:187], v56, s[8:9] offset:320
	v_mfma_f32_16x16x32_bf16 v[120:123], v[228:231], v[208:211], v[120:123]
	v_mfma_f32_16x16x32_bf16 v[124:127], v[228:231], v[212:215], v[124:127]
	global_load_dwordx4 v[188:191], v57, s[8:9] offset:320
	v_mfma_f32_16x16x32_bf16 v[128:131], v[232:235], v[200:203], v[128:131]
	v_mfma_f32_16x16x32_bf16 v[132:135], v[232:235], v[204:207], v[132:135]
	global_load_dwordx4 v[192:195], v58, s[8:9] offset:320
	v_mfma_f32_16x16x32_bf16 v[136:139], v[232:235], v[208:211], v[136:139]
	v_mfma_f32_16x16x32_bf16 v[140:143], v[232:235], v[212:215], v[140:143]
	global_load_dwordx4 v[196:199], v59, s[8:9] offset:320
	v_mfma_f32_16x16x32_bf16 v[144:147], v[236:239], v[200:203], v[144:147]
	v_mfma_f32_16x16x32_bf16 v[148:151], v[236:239], v[204:207], v[148:151]
	v_mfma_f32_16x16x32_bf16 v[152:155], v[236:239], v[208:211], v[152:155]
	v_mfma_f32_16x16x32_bf16 v[156:159], v[236:239], v[212:215], v[156:159]
	s_waitcnt vmcnt(23)
	v_pk_add_f32 v[64:65], v[64:65], v[16:17]
	v_pk_add_f32 v[66:67], v[66:67], v[18:19]
	global_store_dwordx4 v56, v[64:67], s[10:11] offset:0
	s_waitcnt vmcnt(23)
	v_pk_add_f32 v[68:69], v[68:69], v[20:21]
	v_pk_add_f32 v[70:71], v[70:71], v[22:23]
	global_store_dwordx4 v57, v[68:71], s[10:11] offset:0
	s_waitcnt vmcnt(23)
	v_pk_add_f32 v[72:73], v[72:73], v[24:25]
	v_pk_add_f32 v[74:75], v[74:75], v[26:27]
	global_store_dwordx4 v58, v[72:75], s[10:11] offset:0
	s_waitcnt vmcnt(23)
	v_pk_add_f32 v[76:77], v[76:77], v[28:29]
	v_pk_add_f32 v[78:79], v[78:79], v[30:31]
	global_store_dwordx4 v59, v[76:79], s[10:11] offset:0
	s_waitcnt vmcnt(23)
	v_pk_add_f32 v[80:81], v[80:81], v[32:33]
	v_pk_add_f32 v[82:83], v[82:83], v[34:35]
	global_store_dwordx4 v56, v[80:83], s[10:11] offset:64
	s_waitcnt vmcnt(23)
	v_pk_add_f32 v[84:85], v[84:85], v[36:37]
	v_pk_add_f32 v[86:87], v[86:87], v[38:39]
	global_store_dwordx4 v57, v[84:87], s[10:11] offset:64
	s_waitcnt vmcnt(23)
	v_pk_add_f32 v[88:89], v[88:89], v[40:41]
	v_pk_add_f32 v[90:91], v[90:91], v[42:43]
	global_store_dwordx4 v58, v[88:91], s[10:11] offset:64
	s_waitcnt vmcnt(23)
	v_pk_add_f32 v[92:93], v[92:93], v[44:45]
	v_pk_add_f32 v[94:95], v[94:95], v[46:47]
	global_store_dwordx4 v59, v[92:95], s[10:11] offset:64
	s_waitcnt vmcnt(23)
	v_pk_add_f32 v[96:97], v[96:97], v[48:49]
	v_pk_add_f32 v[98:99], v[98:99], v[50:51]
	global_store_dwordx4 v56, v[96:99], s[10:11] offset:128
	s_waitcnt vmcnt(23)
	v_pk_add_f32 v[100:101], v[100:101], v[52:53]
	v_pk_add_f32 v[102:103], v[102:103], v[54:55]
	global_store_dwordx4 v57, v[100:103], s[10:11] offset:128
	s_waitcnt vmcnt(23)
	v_pk_add_f32 v[104:105], v[104:105], v[240:241]
	v_pk_add_f32 v[106:107], v[106:107], v[242:243]
	global_store_dwordx4 v58, v[104:107], s[10:11] offset:128
	s_waitcnt vmcnt(23)
	v_pk_add_f32 v[108:109], v[108:109], v[244:245]
	v_pk_add_f32 v[110:111], v[110:111], v[246:247]
	global_store_dwordx4 v59, v[108:111], s[10:11] offset:128
	s_waitcnt vmcnt(23)
	v_pk_add_f32 v[112:113], v[112:113], v[248:249]
	v_pk_add_f32 v[114:115], v[114:115], v[250:251]
	global_store_dwordx4 v56, v[112:115], s[10:11] offset:192
	s_waitcnt vmcnt(23)
	v_pk_add_f32 v[116:117], v[116:117], v[252:253]
	v_pk_add_f32 v[118:119], v[118:119], v[254:255]
	global_store_dwordx4 v57, v[116:119], s[10:11] offset:192
	s_waitcnt vmcnt(23)
	v_pk_add_f32 v[120:121], v[120:121], v[160:161]
	v_pk_add_f32 v[122:123], v[122:123], v[162:163]
	global_store_dwordx4 v58, v[120:123], s[10:11] offset:192
	s_waitcnt vmcnt(23)
	v_pk_add_f32 v[124:125], v[124:125], v[164:165]
	v_pk_add_f32 v[126:127], v[126:127], v[166:167]
	global_store_dwordx4 v59, v[124:127], s[10:11] offset:192
	s_waitcnt vmcnt(23)
	v_pk_add_f32 v[128:129], v[128:129], v[168:169]
	v_pk_add_f32 v[130:131], v[130:131], v[170:171]
	global_store_dwordx4 v56, v[128:131], s[10:11] offset:256
	s_waitcnt vmcnt(23)
	v_pk_add_f32 v[132:133], v[132:133], v[172:173]
	v_pk_add_f32 v[134:135], v[134:135], v[174:175]
	global_store_dwordx4 v57, v[132:135], s[10:11] offset:256
	s_waitcnt vmcnt(23)
	v_pk_add_f32 v[136:137], v[136:137], v[176:177]
	v_pk_add_f32 v[138:139], v[138:139], v[178:179]
	global_store_dwordx4 v58, v[136:139], s[10:11] offset:256
	s_waitcnt vmcnt(23)
	v_pk_add_f32 v[140:141], v[140:141], v[180:181]
	v_pk_add_f32 v[142:143], v[142:143], v[182:183]
	global_store_dwordx4 v59, v[140:143], s[10:11] offset:256
	s_waitcnt vmcnt(23)
	v_pk_add_f32 v[144:145], v[144:145], v[184:185]
	v_pk_add_f32 v[146:147], v[146:147], v[186:187]
	global_store_dwordx4 v56, v[144:147], s[10:11] offset:320
	s_waitcnt vmcnt(23)
	v_pk_add_f32 v[148:149], v[148:149], v[188:189]
	v_pk_add_f32 v[150:151], v[150:151], v[190:191]
	global_store_dwordx4 v57, v[148:151], s[10:11] offset:320
	s_waitcnt vmcnt(23)
	v_pk_add_f32 v[152:153], v[152:153], v[192:193]
	v_pk_add_f32 v[154:155], v[154:155], v[194:195]
	global_store_dwordx4 v58, v[152:155], s[10:11] offset:320
	s_waitcnt vmcnt(23)
	v_pk_add_f32 v[156:157], v[156:157], v[196:197]
	v_pk_add_f32 v[158:159], v[158:159], v[198:199]
	global_store_dwordx4 v59, v[156:159], s[10:11] offset:320
